# speedup vs baseline: 1.0039x; 1.0039x over previous
.LBB1_33:
	s_mov_b32 s5, 0
	v_lshl_add_u64 v[168:169], v[154:155], 0, s[4:5]
	global_load_dwordx4 v[154:157], v[168:169], off
	ds_read_b128 v[50:53], v179 offset:33792
	ds_read_b128 v[54:57], v179 offset:33824
	ds_read_b128 v[58:61], v179 offset:33856
	ds_read_b128 v[62:65], v179 offset:33888
	ds_read_b128 v[180:183], v179 offset:33920
	ds_read_b128 v[184:187], v179 offset:33952
	s_waitcnt lgkmcnt(5)
	v_mfma_f32_32x32x16_f16 v[34:49], v[122:125], v[50:53], v[2:17]
	ds_read_b128 v[190:193], v179 offset:33984
	v_cvt_pk_f16_f32 v174, v18, v19
	v_cvt_pk_f16_f32 v175, v20, v21
	s_waitcnt lgkmcnt(5)
	v_mfma_f32_32x32x16_f16 v[34:49], v[98:101], v[54:57], v[34:49]
	ds_read_b128 v[18:21], v179 offset:34016
	v_exp_f16_e64 v50, v174 clamp
	v_exp_f16_e64 v51, v175 clamp
	v_exp_f16_sdwa v50, v174 clamp dst_sel:WORD_1 dst_unused:UNUSED_PRESERVE src0_sel:WORD_1
	v_exp_f16_sdwa v51, v175 clamp dst_sel:WORD_1 dst_unused:UNUSED_PRESERVE src0_sel:WORD_1
	s_nop 0
	s_waitcnt lgkmcnt(5)
	v_mfma_f32_32x32x16_f16 v[34:49], v[114:117], v[58:61], v[34:49]
	ds_read_b128 v[194:197], v179 offset:34048
	s_movk_i32 s5, 0x3dc5
	v_mov_b32_e32 v188, 0xbdc5
	v_pk_fma_f16 v51, v51, s5, v188 op_sel_hi:[1,0,0]
	v_pk_fma_f16 v50, v50, s5, v188 op_sel_hi:[1,0,0]
	v_pk_max_f16 v51, v175, v51
	v_pk_max_f16 v50, v174, v50
	s_waitcnt lgkmcnt(5)
	v_mfma_f32_32x32x16_f16 v[34:49], v[86:89], v[62:65], v[34:49]
	ds_read_b128 v[200:203], v179 offset:34080
	v_cvt_pk_f16_f32 v52, v22, v23
	v_cvt_pk_f16_f32 v53, v24, v25
	s_waitcnt lgkmcnt(5)
	v_mfma_f32_32x32x16_f16 v[34:49], v[126:129], v[180:183], v[34:49]
	ds_read_b128 v[22:25], v179 offset:34112
	v_exp_f16_e64 v54, v52 clamp
	v_exp_f16_e64 v55, v53 clamp
	v_exp_f16_sdwa v54, v52 clamp dst_sel:WORD_1 dst_unused:UNUSED_PRESERVE src0_sel:WORD_1
	v_exp_f16_sdwa v55, v53 clamp dst_sel:WORD_1 dst_unused:UNUSED_PRESERVE src0_sel:WORD_1
	s_nop 0
	s_waitcnt lgkmcnt(5)
	v_mfma_f32_32x32x16_f16 v[34:49], v[90:93], v[184:187], v[34:49]
	ds_read_b128 v[180:183], v179 offset:34144
	v_pk_fma_f16 v55, v55, s5, v188 op_sel_hi:[1,0,0]
	v_pk_fma_f16 v54, v54, s5, v188 op_sel_hi:[1,0,0]
	v_pk_max_f16 v53, v53, v55
	v_pk_max_f16 v52, v52, v54
	s_waitcnt lgkmcnt(5)
	v_mfma_f32_32x32x16_f16 v[34:49], v[118:121], v[190:193], v[34:49]
	ds_read_b128 v[184:187], v179 offset:34176
	v_cvt_pk_f16_f32 v174, v26, v27
	v_cvt_pk_f16_f32 v175, v28, v29
	v_mfma_f32_16x16x32_f16 v[62:65], v[70:73], v[50:53], 0
	s_waitcnt lgkmcnt(5)
	v_mfma_f32_32x32x16_f16 v[34:49], v[78:81], v[18:21], v[34:49]
	ds_read_b128 v[26:29], v179 offset:34208
	v_exp_f16_e64 v190, v174 clamp
	v_exp_f16_e64 v191, v175 clamp
	v_exp_f16_sdwa v190, v174 clamp dst_sel:WORD_1 dst_unused:UNUSED_PRESERVE src0_sel:WORD_1
	v_exp_f16_sdwa v191, v175 clamp dst_sel:WORD_1 dst_unused:UNUSED_PRESERVE src0_sel:WORD_1
	s_nop 0
	s_waitcnt lgkmcnt(5)
	v_mfma_f32_32x32x16_f16 v[34:49], v[102:105], v[194:197], v[34:49]
	ds_read_b128 v[18:21], v179 offset:34240
	v_pk_fma_f16 v191, v191, s5, v188 op_sel_hi:[1,0,0]
	s_nop 0
	v_pk_max_f16 v191, v175, v191
	v_pk_fma_f16 v175, v190, s5, v188 op_sel_hi:[1,0,0]
	s_nop 0
	v_pk_max_f16 v190, v174, v175
	s_waitcnt lgkmcnt(5)
	v_mfma_f32_32x32x16_f16 v[34:49], v[74:77], v[200:203], v[34:49]
	ds_read_b128 v[194:197], v179 offset:34272
	v_cvt_pk_f16_f32 v30, v30, v31
	v_cvt_pk_f16_f32 v31, v32, v33
	s_waitcnt lgkmcnt(5)
	v_mfma_f32_32x32x16_f16 v[34:49], v[106:109], v[22:25], v[34:49]
	v_exp_f16_e64 v32, v30 clamp
	v_exp_f16_e64 v33, v31 clamp
	v_exp_f16_sdwa v32, v30 clamp dst_sel:WORD_1 dst_unused:UNUSED_PRESERVE src0_sel:WORD_1
	v_exp_f16_sdwa v33, v31 clamp dst_sel:WORD_1 dst_unused:UNUSED_PRESERVE src0_sel:WORD_1
	s_nop 0
	s_waitcnt lgkmcnt(4)
	v_mfma_f32_32x32x16_f16 v[34:49], v[82:85], v[180:183], v[34:49]
	v_pk_fma_f16 v22, v33, s5, v188 op_sel_hi:[1,0,0]
	s_nop 0
	v_pk_max_f16 v193, v31, v22
	v_pk_fma_f16 v22, v32, s5, v188 op_sel_hi:[1,0,0]
	s_nop 0
	v_pk_max_f16 v192, v30, v22
	s_waitcnt lgkmcnt(3)
	v_mfma_f32_32x32x16_f16 v[34:49], v[110:113], v[184:187], v[34:49]
	s_waitcnt vmcnt(2)
	v_pk_add_f16 v24, v158, v146
	v_pk_add_f16 v25, v159, v147
	s_nop 0
	v_pk_mul_f16 v22, v160, v148 clamp
	v_pk_mul_f16 v23, v161, v149 clamp
	v_pk_max_f16 v22, v24, v22
	v_pk_max_f16 v23, v25, v23
	ds_write_b64 v189, v[22:23]
	v_mfma_f32_16x16x32_f16 v[62:65], v[66:69], v[190:193], v[62:65]
	s_waitcnt lgkmcnt(3)
	v_mfma_f32_32x32x16_f16 v[34:49], v[94:97], v[26:29], v[34:49]
	v_pk_add_f16 v24, v158, v138
	v_pk_add_f16 v25, v159, v139
	s_nop 0
	v_pk_mul_f16 v22, v160, v140 clamp
	v_pk_mul_f16 v23, v161, v141 clamp
	v_pk_max_f16 v22, v24, v22
	v_pk_max_f16 v23, v25, v23
	ds_write_b64 v189, v[22:23] offset:528
	s_waitcnt lgkmcnt(3)
	v_mfma_f32_32x32x16_f16 v[34:49], v[134:137], v[18:21], v[34:49]
	v_pk_add_f16 v24, v158, v150
	v_pk_add_f16 v25, v159, v151
	s_nop 0
	v_pk_mul_f16 v22, v160, v152 clamp
	v_pk_mul_f16 v23, v161, v153 clamp
	v_pk_max_f16 v22, v24, v22
	v_pk_max_f16 v23, v25, v23
	ds_write_b64 v189, v[22:23] offset:1056
	s_waitcnt lgkmcnt(3)
	v_mfma_f32_32x32x16_f16 v[34:49], v[130:133], v[194:197], v[34:49]
	v_pk_add_f16 v20, v158, v142
	v_pk_add_f16 v21, v159, v143
	s_nop 0
	v_pk_mul_f16 v18, v160, v144 clamp
	v_pk_mul_f16 v19, v161, v145 clamp
	v_pk_max_f16 v18, v20, v18
	v_pk_max_f16 v19, v21, v19
	ds_write_b64 v189, v[18:19] offset:1584
	v_mov_b32_e32 v18, 0x12400
	v_lshl_add_u32 v201, v170, 2, v18
	v_mov_b32_e32 v18, 0x12408
	v_lshl_add_u32 v18, v167, 2, v18
	s_mov_b32 s5, 0x12400
	v_add3_u32 v18, v171, v172, s5
	ds_write2_b32 v201, v62, v63 offset1:1
	s_and_saveexec_b64 s[6:7], s[0:1]
	ds_write2_b32 v201, v64, v65 offset0:2 offset1:3
	s_or_b64 exec, exec, s[6:7]
	s_mov_b32 s5, 0
	v_lshl_add_u64 v[168:169], v[168:169], 0, s[4:5]
	global_load_dwordx4 v[158:161], v[168:169], off
	ds_read_b128 v[50:53], v179 offset:50688
	ds_read_b128 v[54:57], v179 offset:50720
	ds_read_b128 v[58:61], v179 offset:50752
	ds_read_b128 v[62:65], v179 offset:50784
	ds_read_b128 v[180:183], v179 offset:50816
	ds_read_b128 v[184:187], v179 offset:50848
	s_waitcnt lgkmcnt(5)
	v_mfma_f32_32x32x16_f16 v[18:33], v[122:125], v[50:53], v[2:17]
	ds_read_b128 v[190:193], v179 offset:50880
	v_cvt_pk_f16_f32 v174, v34, v35
	v_cvt_pk_f16_f32 v175, v36, v37
	s_waitcnt lgkmcnt(5)
	v_mfma_f32_32x32x16_f16 v[18:33], v[98:101], v[54:57], v[18:33]
	ds_read_b128 v[34:37], v179 offset:50912
	v_exp_f16_e64 v50, v174 clamp
	v_exp_f16_e64 v51, v175 clamp
	v_exp_f16_sdwa v50, v174 clamp dst_sel:WORD_1 dst_unused:UNUSED_PRESERVE src0_sel:WORD_1
	v_exp_f16_sdwa v51, v175 clamp dst_sel:WORD_1 dst_unused:UNUSED_PRESERVE src0_sel:WORD_1
	s_nop 0
	s_waitcnt lgkmcnt(5)
	v_mfma_f32_32x32x16_f16 v[18:33], v[114:117], v[58:61], v[18:33]
	ds_read_b128 v[194:197], v179 offset:50944
	s_movk_i32 s5, 0x3dc5
	v_mov_b32_e32 v188, 0xbdc5
	v_pk_fma_f16 v51, v51, s5, v188 op_sel_hi:[1,0,0]
	v_pk_fma_f16 v50, v50, s5, v188 op_sel_hi:[1,0,0]
	v_pk_max_f16 v51, v175, v51
	v_pk_max_f16 v50, v174, v50
	s_waitcnt lgkmcnt(5)
	v_mfma_f32_32x32x16_f16 v[18:33], v[86:89], v[62:65], v[18:33]
	ds_read_b128 v[202:205], v179 offset:50976
	v_cvt_pk_f16_f32 v52, v38, v39
	v_cvt_pk_f16_f32 v53, v40, v41
	s_waitcnt lgkmcnt(5)
	v_mfma_f32_32x32x16_f16 v[18:33], v[126:129], v[180:183], v[18:33]
	ds_read_b128 v[38:41], v179 offset:51008
	v_exp_f16_e64 v54, v52 clamp
	v_exp_f16_e64 v55, v53 clamp
	v_exp_f16_sdwa v54, v52 clamp dst_sel:WORD_1 dst_unused:UNUSED_PRESERVE src0_sel:WORD_1
	v_exp_f16_sdwa v55, v53 clamp dst_sel:WORD_1 dst_unused:UNUSED_PRESERVE src0_sel:WORD_1
	s_nop 0
	s_waitcnt lgkmcnt(5)
	v_mfma_f32_32x32x16_f16 v[18:33], v[90:93], v[184:187], v[18:33]
	ds_read_b128 v[180:183], v179 offset:51040
	v_pk_fma_f16 v55, v55, s5, v188 op_sel_hi:[1,0,0]
	v_pk_fma_f16 v54, v54, s5, v188 op_sel_hi:[1,0,0]
	v_pk_max_f16 v53, v53, v55
	v_pk_max_f16 v52, v52, v54
	s_waitcnt lgkmcnt(5)
	v_mfma_f32_32x32x16_f16 v[18:33], v[118:121], v[190:193], v[18:33]
	ds_read_b128 v[184:187], v179 offset:51072
	v_cvt_pk_f16_f32 v174, v42, v43
	v_cvt_pk_f16_f32 v175, v44, v45
	v_mfma_f32_16x16x32_f16 v[62:65], v[70:73], v[50:53], 0
	s_waitcnt lgkmcnt(5)
	v_mfma_f32_32x32x16_f16 v[18:33], v[78:81], v[34:37], v[18:33]
	ds_read_b128 v[42:45], v179 offset:51104
	v_exp_f16_e64 v190, v174 clamp
	v_exp_f16_e64 v191, v175 clamp
	v_exp_f16_sdwa v190, v174 clamp dst_sel:WORD_1 dst_unused:UNUSED_PRESERVE src0_sel:WORD_1
	v_exp_f16_sdwa v191, v175 clamp dst_sel:WORD_1 dst_unused:UNUSED_PRESERVE src0_sel:WORD_1
	s_nop 0
	s_waitcnt lgkmcnt(5)
	v_mfma_f32_32x32x16_f16 v[18:33], v[102:105], v[194:197], v[18:33]
	ds_read_b128 v[34:37], v179 offset:51136
	v_pk_fma_f16 v191, v191, s5, v188 op_sel_hi:[1,0,0]
	s_nop 0
	v_pk_max_f16 v191, v175, v191
	v_pk_fma_f16 v175, v190, s5, v188 op_sel_hi:[1,0,0]
	s_nop 0
	v_pk_max_f16 v190, v174, v175
	s_waitcnt lgkmcnt(5)
	v_mfma_f32_32x32x16_f16 v[18:33], v[74:77], v[202:205], v[18:33]
	ds_read_b128 v[194:197], v179 offset:51168
	v_cvt_pk_f16_f32 v46, v46, v47
	v_cvt_pk_f16_f32 v47, v48, v49
	s_waitcnt lgkmcnt(5)
	v_mfma_f32_32x32x16_f16 v[18:33], v[106:109], v[38:41], v[18:33]
	v_exp_f16_e64 v48, v46 clamp
	v_exp_f16_e64 v49, v47 clamp
	v_exp_f16_sdwa v48, v46 clamp dst_sel:WORD_1 dst_unused:UNUSED_PRESERVE src0_sel:WORD_1
	v_exp_f16_sdwa v49, v47 clamp dst_sel:WORD_1 dst_unused:UNUSED_PRESERVE src0_sel:WORD_1
	s_nop 0
	s_waitcnt lgkmcnt(4)
	v_mfma_f32_32x32x16_f16 v[18:33], v[82:85], v[180:183], v[18:33]
	v_pk_fma_f16 v38, v49, s5, v188 op_sel_hi:[1,0,0]
	s_nop 0
	v_pk_max_f16 v193, v47, v38
	v_pk_fma_f16 v38, v48, s5, v188 op_sel_hi:[1,0,0]
	s_nop 0
	v_pk_max_f16 v192, v46, v38
	s_waitcnt lgkmcnt(3)
	v_mfma_f32_32x32x16_f16 v[18:33], v[110:113], v[184:187], v[18:33]
	s_waitcnt vmcnt(2)
	v_pk_add_f16 v40, v162, v146
	v_pk_add_f16 v41, v163, v147
	s_nop 0
	v_pk_mul_f16 v38, v164, v148 clamp
	v_pk_mul_f16 v39, v165, v149 clamp
	v_pk_max_f16 v38, v40, v38
	v_pk_max_f16 v39, v41, v39
	ds_write_b64 v189, v[38:39] offset:16896
	v_mfma_f32_16x16x32_f16 v[62:65], v[66:69], v[190:193], v[62:65]
	s_waitcnt lgkmcnt(3)
	v_mfma_f32_32x32x16_f16 v[18:33], v[94:97], v[42:45], v[18:33]
	v_pk_add_f16 v40, v162, v138
	v_pk_add_f16 v41, v163, v139
	s_nop 0
	v_pk_mul_f16 v38, v164, v140 clamp
	v_pk_mul_f16 v39, v165, v141 clamp
	v_pk_max_f16 v38, v40, v38
	v_pk_max_f16 v39, v41, v39
	ds_write_b64 v189, v[38:39] offset:17424
	s_waitcnt lgkmcnt(3)
	v_mfma_f32_32x32x16_f16 v[18:33], v[134:137], v[34:37], v[18:33]
	v_pk_add_f16 v40, v162, v150
	v_pk_add_f16 v41, v163, v151
	s_nop 0
	v_pk_mul_f16 v38, v164, v152 clamp
	v_pk_mul_f16 v39, v165, v153 clamp
	v_pk_max_f16 v38, v40, v38
	v_pk_max_f16 v39, v41, v39
	ds_write_b64 v189, v[38:39] offset:17952
	s_waitcnt lgkmcnt(3)
	v_mfma_f32_32x32x16_f16 v[18:33], v[130:133], v[194:197], v[18:33]
	v_pk_add_f16 v36, v162, v142
	v_pk_add_f16 v37, v163, v143
	s_nop 0
	v_pk_mul_f16 v34, v164, v144 clamp
	v_pk_mul_f16 v35, v165, v145 clamp
	v_pk_max_f16 v34, v36, v34
	v_pk_max_f16 v35, v37, v35
	ds_write_b64 v189, v[34:35] offset:18480
	v_mov_b32_e32 v34, 0x14000
	v_lshl_add_u32 v211, v170, 2, v34
	v_mov_b32_e32 v34, 0x14008
	v_lshl_add_u32 v34, v167, 2, v34
	s_mov_b32 s5, 0x14000
	v_add3_u32 v34, v171, v172, s5
	ds_write2_b32 v211, v62, v63 offset1:1
	s_and_saveexec_b64 s[6:7], s[0:1]
	ds_write2_b32 v211, v64, v65 offset0:2 offset1:3
	s_or_b64 exec, exec, s[6:7]
	s_mov_b32 s21, 0
	s_mov_b32 s5, s21
	v_lshl_add_u64 v[168:169], v[168:169], 0, s[4:5]
	s_sub_i32 s4, 0x7e, s28
	s_mul_i32 s4, s4, 6
	s_ashr_i32 s5, s4, 31
	s_add_u32 s26, s8, s4
	s_addc_u32 s27, s9, s5
	s_or_b32 s31, s28, 1
	s_or_b64 s[4:5], s[18:19], s[22:23]
	s_and_b64 s[4:5], s[4:5], exec
	s_cselect_b32 s6, s13, s46
	s_cselect_b32 s7, s12, s45
	s_lshl_b32 s4, s30, 6
	s_ashr_i32 s5, s4, 31
	s_lshl_b64 s[4:5], s[4:5], 4
	s_add_u32 s4, s7, s4
	s_addc_u32 s5, s6, s5
	s_lshl_b32 s51, s29, 4
	s_sub_i32 s9, 0xff, s51
	s_mul_i32 s9, s9, s51
	s_sub_i32 s28, s43, s29
	s_ashr_i32 s9, s9, 1
	s_lshl_b32 s28, s28, 4
	s_add_i32 s9, s28, s9
	s_add_i32 s9, s9, -1
	s_mul_i32 s8, s33, 0x1fc0
	s_ashr_i32 s28, s9, 31
	v_mov_b32_e32 v167, 0
	v_lshlrev_b32_e32 v34, 2, v173
	s_add_u32 s8, s9, s8
	v_lshl_add_u64 v[174:175], s[4:5], 0, v[166:167]
	v_cndmask_b32_e64 v231, 0, 1, s[16:17]
	s_movk_i32 s4, 0xc0
	v_add_u32_e32 v200, 0x12400, v34
	s_addc_u32 s9, s28, 0
	v_add_u32_e32 v190, 0x14000, v34
	v_add_u32_e32 v180, 0x15c00, v34
	v_add_u32_e32 v216, 0x10800, v34
	v_add_u32_e32 v209, 0x125c0, v34
	v_add_u32_e32 v210, 0x12940, v34
	v_add_u32_e32 v207, 0x12cc0, v34
	v_add_u32_e32 v208, 0x13040, v34
	v_add_u32_e32 v204, 0x133c0, v34
	v_add_u32_e32 v205, 0x13740, v34
	v_add_u32_e32 v202, 0x13ac0, v34
	v_add_u32_e32 v203, 0x13e40, v34
	v_add_u32_e32 v197, 0x141c0, v34
	v_add_u32_e32 v198, 0x14540, v34
	v_add_u32_e32 v195, 0x148c0, v34
	v_add_u32_e32 v196, 0x14c40, v34
	v_add_u32_e32 v193, 0x14fc0, v34
	v_add_u32_e32 v194, 0x15340, v34
	v_add_u32_e32 v191, 0x156c0, v34
	v_add_u32_e32 v192, 0x15a40, v34
	v_add_u32_e32 v187, 0x15dc0, v34
	v_add_u32_e32 v188, 0x16140, v34
	v_add_u32_e32 v185, 0x164c0, v34
	v_add_u32_e32 v186, 0x16840, v34
	v_add_u32_e32 v183, 0x16bc0, v34
	v_add_u32_e32 v184, 0x16f40, v34
	v_add_u32_e32 v181, 0x172c0, v34
	v_add_u32_e32 v182, 0x17640, v34
	v_add_u32_e32 v223, 0x109c0, v34
	v_add_u32_e32 v224, 0x10d40, v34
	v_add_u32_e32 v221, 0x110c0, v34
	v_add_u32_e32 v222, 0x11440, v34
	v_add_u32_e32 v219, 0x117c0, v34
	v_add_u32_e32 v220, 0x11b40, v34
	v_add_u32_e32 v217, 0x11ec0, v34
	v_add_u32_e32 v218, 0x12240, v34
	v_mov_b32_e32 v34, 0x17800
	v_cndmask_b32_e64 v230, 0, 1, s[18:19]
	v_readfirstlane_b32 s50, v231
	v_cmp_gt_u32_e64 s[6:7], s4, v0
	s_movk_i32 s4, 0x60
	s_mul_i32 s9, s9, 6
	s_mul_hi_u32 s28, s8, 6
	v_mov_b32_e32 v35, 0x15c00
	v_add_u32_e32 v228, 0x15c00, v171
	v_add_u32_e32 v226, 0x10800, v171
	v_add_u32_e32 v215, 0x12400, v171
	v_add_u32_e32 v213, 0x14000, v171
	v_lshl_add_u32 v232, v177, 2, v34
	v_cndmask_b32_e64 v34, 0, 1, s[24:25]
	s_mov_b32 s48, 1
	v_readfirstlane_b32 s49, v230
	v_cmp_gt_u32_e64 s[4:5], s4, v0
	s_add_i32 s52, s28, s9
	s_mul_i32 s53, s8, 6
	v_lshl_add_u32 v229, v170, 2, v35
	v_add_u32_e32 v227, v228, v172
	v_add_u32_e32 v225, v226, v172
	v_add_u32_e32 v214, v215, v172
	v_add_u32_e32 v212, v213, v172
	s_mov_b32 s56, 8
	s_mov_b32 s54, 16
	v_cmp_ne_u32_e64 s[8:9], 1, v34
	s_movk_i32 s55, 0x3dc5
	v_mov_b32_e32 v233, 0xbdc5
	v_add_u32_e32 v234, 0x700, v200
	v_add_u32_e32 v235, 0xe00, v200
	v_add_u32_e32 v236, 0x1500, v200
	v_add_u32_e32 v237, 0x700, v190
	v_add_u32_e32 v238, 0xe00, v190
	v_add_u32_e32 v239, 0x1500, v190
	s_mov_b32 s41, s50
	s_waitcnt lgkmcnt(0)
	s_barrier
	ds_read_b128 v[50:53], v179
	s_and_b64 vcc, exec, s[8:9]
	s_cbranch_vccnz .LBB1_50

.LBB1_59:
	global_load_dwordx4 v[162:165], v[168:169], off
	ds_read_b128 v[54:57], v179 offset:32
	ds_read_b128 v[58:61], v179 offset:64
	ds_read_b128 v[62:65], v179 offset:96
	ds_read_b128 v[170:173], v179 offset:128
	ds_read_b128 v[240:243], v179 offset:160
	s_waitcnt lgkmcnt(5)
	v_mfma_f32_32x32x16_f16 v[34:49], v[122:125], v[50:53], v[2:17]
	ds_read_b128 v[244:247], v179 offset:192
	v_cvt_pk_f16_f32 v166, v18, v19
	v_cvt_pk_f16_f32 v167, v20, v21
	s_waitcnt lgkmcnt(5)
	v_mfma_f32_32x32x16_f16 v[34:49], v[98:101], v[54:57], v[34:49]
	ds_read_b128 v[18:21], v179 offset:224
	v_exp_f16_e64 v50, v166 clamp
	v_exp_f16_e64 v51, v167 clamp
	v_exp_f16_sdwa v50, v166 clamp dst_sel:WORD_1 dst_unused:UNUSED_PRESERVE src0_sel:WORD_1
	v_exp_f16_sdwa v51, v167 clamp dst_sel:WORD_1 dst_unused:UNUSED_PRESERVE src0_sel:WORD_1
	s_nop 0
	s_waitcnt lgkmcnt(5)
	v_mfma_f32_32x32x16_f16 v[34:49], v[114:117], v[58:61], v[34:49]
	ds_read_b128 v[248:251], v179 offset:256
	v_pk_fma_f16 v51, v51, s55, v233 op_sel_hi:[1,0,0]
	v_pk_fma_f16 v50, v50, s55, v233 op_sel_hi:[1,0,0]
	v_pk_max_f16 v51, v167, v51
	v_pk_max_f16 v50, v166, v50
	s_waitcnt lgkmcnt(5)
	v_mfma_f32_32x32x16_f16 v[34:49], v[86:89], v[62:65], v[34:49]
	ds_read_b128 v[252:255], v179 offset:288
	v_cvt_pk_f16_f32 v52, v22, v23
	v_cvt_pk_f16_f32 v53, v24, v25
	s_waitcnt lgkmcnt(5)
	v_mfma_f32_32x32x16_f16 v[34:49], v[126:129], v[170:173], v[34:49]
	ds_read_b128 v[22:25], v179 offset:320
	v_exp_f16_e64 v54, v52 clamp
	v_exp_f16_e64 v55, v53 clamp
	v_exp_f16_sdwa v54, v52 clamp dst_sel:WORD_1 dst_unused:UNUSED_PRESERVE src0_sel:WORD_1
	v_exp_f16_sdwa v55, v53 clamp dst_sel:WORD_1 dst_unused:UNUSED_PRESERVE src0_sel:WORD_1
	s_nop 0
	s_waitcnt lgkmcnt(5)
	v_mfma_f32_32x32x16_f16 v[34:49], v[90:93], v[240:243], v[34:49]
	ds_read_b128 v[170:173], v179 offset:352
	v_pk_fma_f16 v55, v55, s55, v233 op_sel_hi:[1,0,0]
	v_pk_fma_f16 v54, v54, s55, v233 op_sel_hi:[1,0,0]
	v_pk_max_f16 v53, v53, v55
	v_pk_max_f16 v52, v52, v54
	s_waitcnt lgkmcnt(5)
	v_mfma_f32_32x32x16_f16 v[34:49], v[118:121], v[244:247], v[34:49]
	ds_read_b128 v[240:243], v179 offset:384
	v_cvt_pk_f16_f32 v166, v26, v27
	v_cvt_pk_f16_f32 v167, v28, v29
	v_mfma_f32_16x16x32_f16 v[62:65], v[70:73], v[50:53], 0
	s_waitcnt lgkmcnt(5)
	v_mfma_f32_32x32x16_f16 v[34:49], v[78:81], v[18:21], v[34:49]
	ds_read_b128 v[26:29], v179 offset:416
	v_exp_f16_e64 v244, v166 clamp
	v_exp_f16_e64 v245, v167 clamp
	v_exp_f16_sdwa v244, v166 clamp dst_sel:WORD_1 dst_unused:UNUSED_PRESERVE src0_sel:WORD_1
	v_exp_f16_sdwa v245, v167 clamp dst_sel:WORD_1 dst_unused:UNUSED_PRESERVE src0_sel:WORD_1
	s_nop 0
	s_waitcnt lgkmcnt(5)
	v_mfma_f32_32x32x16_f16 v[34:49], v[102:105], v[248:251], v[34:49]
	ds_read_b128 v[18:21], v179 offset:448
	v_pk_fma_f16 v245, v245, s55, v233 op_sel_hi:[1,0,0]
	s_nop 0
	v_pk_max_f16 v245, v167, v245
	v_pk_fma_f16 v167, v244, s55, v233 op_sel_hi:[1,0,0]
	s_nop 0
	v_pk_max_f16 v244, v166, v167
	s_waitcnt lgkmcnt(5)
	v_mfma_f32_32x32x16_f16 v[34:49], v[74:77], v[252:255], v[34:49]
	ds_read_b128 v[248:251], v179 offset:480
	v_cvt_pk_f16_f32 v30, v30, v31
	v_cvt_pk_f16_f32 v31, v32, v33
	s_waitcnt lgkmcnt(5)
	v_mfma_f32_32x32x16_f16 v[34:49], v[106:109], v[22:25], v[34:49]
	v_exp_f16_e64 v32, v30 clamp
	v_exp_f16_e64 v33, v31 clamp
	v_exp_f16_sdwa v32, v30 clamp dst_sel:WORD_1 dst_unused:UNUSED_PRESERVE src0_sel:WORD_1
	v_exp_f16_sdwa v33, v31 clamp dst_sel:WORD_1 dst_unused:UNUSED_PRESERVE src0_sel:WORD_1
	s_nop 0
	s_waitcnt lgkmcnt(4)
	v_mfma_f32_32x32x16_f16 v[34:49], v[82:85], v[170:173], v[34:49]
	v_pk_fma_f16 v22, v33, s55, v233 op_sel_hi:[1,0,0]
	s_nop 0
	v_pk_max_f16 v247, v31, v22
	v_pk_fma_f16 v22, v32, s55, v233 op_sel_hi:[1,0,0]
	s_nop 0
	v_pk_max_f16 v246, v30, v22
	s_waitcnt lgkmcnt(3)
	v_mfma_f32_32x32x16_f16 v[34:49], v[110:113], v[240:243], v[34:49]
	s_waitcnt vmcnt(2)
	v_pk_add_f16 v24, v154, v146
	v_pk_add_f16 v25, v155, v147
	s_nop 0
	v_pk_mul_f16 v22, v156, v148 clamp
	v_pk_mul_f16 v23, v157, v149 clamp
	v_pk_max_f16 v22, v24, v22
	v_pk_max_f16 v23, v25, v23
	ds_write_b64 v189, v[22:23] offset:33792
	v_mfma_f32_16x16x32_f16 v[62:65], v[66:69], v[244:247], v[62:65]
	s_waitcnt lgkmcnt(3)
	v_mfma_f32_32x32x16_f16 v[34:49], v[94:97], v[26:29], v[34:49]
	v_pk_add_f16 v24, v154, v138
	v_pk_add_f16 v25, v155, v139
	s_nop 0
	v_pk_mul_f16 v22, v156, v140 clamp
	v_pk_mul_f16 v23, v157, v141 clamp
	v_pk_max_f16 v22, v24, v22
	v_pk_max_f16 v23, v25, v23
	ds_write_b64 v189, v[22:23] offset:34320
	s_waitcnt lgkmcnt(3)
	v_mfma_f32_32x32x16_f16 v[34:49], v[134:137], v[18:21], v[34:49]
	v_pk_add_f16 v24, v154, v150
	v_pk_add_f16 v25, v155, v151
	s_nop 0
	v_pk_mul_f16 v22, v156, v152 clamp
	v_pk_mul_f16 v23, v157, v153 clamp
	v_pk_max_f16 v22, v24, v22
	v_pk_max_f16 v23, v25, v23
	ds_write_b64 v189, v[22:23] offset:34848
	s_waitcnt lgkmcnt(3)
	v_mfma_f32_32x32x16_f16 v[34:49], v[130:133], v[248:251], v[34:49]
	v_pk_add_f16 v20, v154, v142
	v_pk_add_f16 v21, v155, v143
	s_nop 0
	v_pk_mul_f16 v18, v156, v144 clamp
	v_pk_mul_f16 v19, v157, v145 clamp
	v_pk_max_f16 v18, v20, v18
	v_pk_max_f16 v19, v21, v19
	ds_write_b64 v189, v[18:19] offset:35376
	ds_write2_b32 v229, v62, v63 offset1:1
	s_and_saveexec_b64 s[28:29], s[0:1]
	ds_write2_b32 v229, v64, v65 offset0:2 offset1:3
	s_or_b64 exec, exec, s[28:29]
	v_lshl_add_u64 v[166:167], s[20:21], 4, v[168:169]
	global_load_dwordx4 v[154:157], v[166:167], off
	ds_read_b128 v[50:53], v179 offset:16896
	ds_read_b128 v[54:57], v179 offset:16928
	ds_read_b128 v[58:61], v179 offset:16960
	ds_read_b128 v[62:65], v179 offset:16992
	ds_read_b128 v[168:171], v179 offset:17024
	ds_read_b128 v[240:243], v179 offset:17056
	s_waitcnt lgkmcnt(5)
	v_mfma_f32_32x32x16_f16 v[18:33], v[122:125], v[50:53], v[2:17]
	ds_read_b128 v[244:247], v179 offset:17088
	v_cvt_pk_f16_f32 v172, v34, v35
	v_cvt_pk_f16_f32 v173, v36, v37
	s_waitcnt lgkmcnt(5)
	v_mfma_f32_32x32x16_f16 v[18:33], v[98:101], v[54:57], v[18:33]
	ds_read_b128 v[34:37], v179 offset:17120
	v_exp_f16_e64 v50, v172 clamp
	v_exp_f16_e64 v51, v173 clamp
	v_exp_f16_sdwa v50, v172 clamp dst_sel:WORD_1 dst_unused:UNUSED_PRESERVE src0_sel:WORD_1
	v_exp_f16_sdwa v51, v173 clamp dst_sel:WORD_1 dst_unused:UNUSED_PRESERVE src0_sel:WORD_1
	s_nop 0
	s_waitcnt lgkmcnt(5)
	v_mfma_f32_32x32x16_f16 v[18:33], v[114:117], v[58:61], v[18:33]
	ds_read_b128 v[248:251], v179 offset:17152
	v_pk_fma_f16 v51, v51, s55, v233 op_sel_hi:[1,0,0]
	v_pk_fma_f16 v50, v50, s55, v233 op_sel_hi:[1,0,0]
	v_pk_max_f16 v51, v173, v51
	v_pk_max_f16 v50, v172, v50
	s_waitcnt lgkmcnt(5)
	v_mfma_f32_32x32x16_f16 v[18:33], v[86:89], v[62:65], v[18:33]
	ds_read_b128 v[252:255], v179 offset:17184
	v_cvt_pk_f16_f32 v52, v38, v39
	v_cvt_pk_f16_f32 v53, v40, v41
	s_waitcnt lgkmcnt(5)
	v_mfma_f32_32x32x16_f16 v[18:33], v[126:129], v[168:171], v[18:33]
	ds_read_b128 v[38:41], v179 offset:17216
	v_exp_f16_e64 v54, v52 clamp
	v_exp_f16_e64 v55, v53 clamp
	v_exp_f16_sdwa v54, v52 clamp dst_sel:WORD_1 dst_unused:UNUSED_PRESERVE src0_sel:WORD_1
	v_exp_f16_sdwa v55, v53 clamp dst_sel:WORD_1 dst_unused:UNUSED_PRESERVE src0_sel:WORD_1
	s_nop 0
	s_waitcnt lgkmcnt(5)
	v_mfma_f32_32x32x16_f16 v[18:33], v[90:93], v[240:243], v[18:33]
	ds_read_b128 v[168:171], v179 offset:17248
	v_pk_fma_f16 v55, v55, s55, v233 op_sel_hi:[1,0,0]
	v_pk_fma_f16 v54, v54, s55, v233 op_sel_hi:[1,0,0]
	v_pk_max_f16 v53, v53, v55
	v_pk_max_f16 v52, v52, v54
	s_waitcnt lgkmcnt(5)
	v_mfma_f32_32x32x16_f16 v[18:33], v[118:121], v[244:247], v[18:33]
	ds_read_b128 v[240:243], v179 offset:17280
	v_cvt_pk_f16_f32 v172, v42, v43
	v_cvt_pk_f16_f32 v173, v44, v45
	v_mfma_f32_16x16x32_f16 v[62:65], v[70:73], v[50:53], 0
	s_waitcnt lgkmcnt(5)
	v_mfma_f32_32x32x16_f16 v[18:33], v[78:81], v[34:37], v[18:33]
	ds_read_b128 v[42:45], v179 offset:17312
	v_exp_f16_e64 v244, v172 clamp
	v_exp_f16_e64 v245, v173 clamp
	v_exp_f16_sdwa v244, v172 clamp dst_sel:WORD_1 dst_unused:UNUSED_PRESERVE src0_sel:WORD_1
	v_exp_f16_sdwa v245, v173 clamp dst_sel:WORD_1 dst_unused:UNUSED_PRESERVE src0_sel:WORD_1
	s_nop 0
	s_waitcnt lgkmcnt(5)
	v_mfma_f32_32x32x16_f16 v[18:33], v[102:105], v[248:251], v[18:33]
	ds_read_b128 v[34:37], v179 offset:17344
	v_pk_fma_f16 v245, v245, s55, v233 op_sel_hi:[1,0,0]
	s_nop 0
	v_pk_max_f16 v245, v173, v245
	v_pk_fma_f16 v173, v244, s55, v233 op_sel_hi:[1,0,0]
	s_nop 0
	v_pk_max_f16 v244, v172, v173
	s_waitcnt lgkmcnt(5)
	v_mfma_f32_32x32x16_f16 v[18:33], v[74:77], v[252:255], v[18:33]
	ds_read_b128 v[248:251], v179 offset:17376
	v_cvt_pk_f16_f32 v46, v46, v47
	v_cvt_pk_f16_f32 v47, v48, v49
	s_waitcnt lgkmcnt(5)
	v_mfma_f32_32x32x16_f16 v[18:33], v[106:109], v[38:41], v[18:33]
	v_exp_f16_e64 v48, v46 clamp
	v_exp_f16_e64 v49, v47 clamp
	v_exp_f16_sdwa v48, v46 clamp dst_sel:WORD_1 dst_unused:UNUSED_PRESERVE src0_sel:WORD_1
	v_exp_f16_sdwa v49, v47 clamp dst_sel:WORD_1 dst_unused:UNUSED_PRESERVE src0_sel:WORD_1
	s_nop 0
	s_waitcnt lgkmcnt(4)
	v_mfma_f32_32x32x16_f16 v[18:33], v[82:85], v[168:171], v[18:33]
	v_pk_fma_f16 v38, v49, s55, v233 op_sel_hi:[1,0,0]
	s_nop 0
	v_pk_max_f16 v247, v47, v38
	v_pk_fma_f16 v38, v48, s55, v233 op_sel_hi:[1,0,0]
	s_nop 0
	v_pk_max_f16 v246, v46, v38
	s_waitcnt lgkmcnt(3)
	v_mfma_f32_32x32x16_f16 v[18:33], v[110:113], v[240:243], v[18:33]
	s_waitcnt vmcnt(2)
	v_pk_add_f16 v40, v158, v146
	v_pk_add_f16 v41, v159, v147
	s_nop 0
	v_pk_mul_f16 v38, v160, v148 clamp
	v_pk_mul_f16 v39, v161, v149 clamp
	v_pk_max_f16 v38, v40, v38
	v_pk_max_f16 v39, v41, v39
	ds_write_b64 v189, v[38:39] offset:50688
	v_mfma_f32_16x16x32_f16 v[62:65], v[66:69], v[244:247], v[62:65]
	s_waitcnt lgkmcnt(3)
	v_mfma_f32_32x32x16_f16 v[18:33], v[94:97], v[42:45], v[18:33]
	v_pk_add_f16 v40, v158, v138
	v_pk_add_f16 v41, v159, v139
	s_nop 0
	v_pk_mul_f16 v38, v160, v140 clamp
	v_pk_mul_f16 v39, v161, v141 clamp
	v_pk_max_f16 v38, v40, v38
	v_pk_max_f16 v39, v41, v39
	ds_write_b64 v189, v[38:39] offset:51216
	s_waitcnt lgkmcnt(3)
	v_mfma_f32_32x32x16_f16 v[18:33], v[134:137], v[34:37], v[18:33]
	v_pk_add_f16 v40, v158, v150
	v_pk_add_f16 v41, v159, v151
	s_nop 0
	v_pk_mul_f16 v38, v160, v152 clamp
	v_pk_mul_f16 v39, v161, v153 clamp
	v_pk_max_f16 v38, v40, v38
	v_pk_max_f16 v39, v41, v39
	ds_write_b64 v189, v[38:39] offset:51744
	s_waitcnt lgkmcnt(3)
	v_mfma_f32_32x32x16_f16 v[18:33], v[130:133], v[248:251], v[18:33]
	v_pk_add_f16 v36, v158, v142
	v_pk_add_f16 v37, v159, v143
	s_nop 0
	v_pk_mul_f16 v34, v160, v144 clamp
	v_pk_mul_f16 v35, v161, v145 clamp
	v_pk_max_f16 v34, v36, v34
	v_pk_max_f16 v35, v37, v35
	ds_write_b64 v189, v[34:35] offset:52272
	ds_write2_b32 v206, v62, v63 offset1:1
	s_and_saveexec_b64 s[28:29], s[0:1]
	ds_write2_b32 v206, v64, v65 offset0:2 offset1:3
	s_or_b64 exec, exec, s[28:29]
	s_sub_i32 s28, 0x7d, s31
	s_mul_i32 s28, s28, 6
	s_ashr_i32 s29, s28, 31
	s_add_u32 s26, s26, s28
	s_addc_u32 s27, s27, s29
	s_and_b64 vcc, exec, s[8:9]
	s_waitcnt lgkmcnt(0)
	s_barrier
	ds_read_b128 v[50:53], v179 offset:33792
	s_cbranch_vccnz .LBB1_76
	s_cmp_lg_u32 s41, 0
	s_cbranch_scc0 .LBB1_72
	s_and_saveexec_b64 s[28:29], s[6:7]
	s_cbranch_execz .LBB1_71
	ds_read2_b32 v[34:35], v180 offset1:224
	v_add_u32_e32 v36, 0x700, v180
	ds_read2_b32 v[36:37], v36 offset1:224
	v_add_u32_e32 v38, 0xe00, v180
	s_lshl_b32 s30, s56, 28
	s_waitcnt lgkmcnt(1)
	v_add_f32_e32 v34, 0, v34
	v_add_f32_e32 v40, v34, v35
	ds_read2_b32 v[34:35], v38 offset1:224
	v_add_u32_e32 v38, 0x1500, v180
	ds_read2_b32 v[38:39], v38 offset1:224
	s_waitcnt lgkmcnt(2)
	v_add_f32_e32 v36, v40, v36
	v_add_f32_e32 v36, v36, v37
	s_waitcnt lgkmcnt(1)
	v_add_f32_e32 v34, v36, v34
	s_add_i32 s30, s30, 0xb0000000
	v_add_f32_e32 v34, v34, v35
	s_ashr_i32 s30, s30, 31
	s_waitcnt lgkmcnt(0)
	v_add_f32_e32 v34, v34, v38
	s_and_b32 s30, s30, 0x1800
	v_add_f32_e32 v34, v34, v39
	v_add_u32_e32 v35, s30, v232
	ds_write_b32 v35, v34 offset:384

.LBB1_93:
	v_lshl_add_u64 v[158:159], s[20:21], 4, v[166:167]
	global_load_dwordx4 v[170:173], v[158:159], off
	ds_read_b128 v[54:57], v179 offset:33824
	ds_read_b128 v[58:61], v179 offset:33856
	ds_read_b128 v[62:65], v179 offset:33888
	ds_read_b128 v[166:169], v179 offset:33920
	ds_read_b128 v[240:243], v179 offset:33952
	s_add_i32 s34, s57, 1
	s_waitcnt lgkmcnt(5)
	v_mfma_f32_32x32x16_f16 v[34:49], v[122:125], v[50:53], v[2:17]
	ds_read_b128 v[244:247], v179 offset:33984
	v_cvt_pk_f16_f32 v160, v18, v19
	v_cvt_pk_f16_f32 v161, v20, v21
	s_waitcnt lgkmcnt(5)
	v_mfma_f32_32x32x16_f16 v[34:49], v[98:101], v[54:57], v[34:49]
	ds_read_b128 v[18:21], v179 offset:34016
	v_exp_f16_e64 v50, v160 clamp
	v_exp_f16_e64 v51, v161 clamp
	v_exp_f16_sdwa v50, v160 clamp dst_sel:WORD_1 dst_unused:UNUSED_PRESERVE src0_sel:WORD_1
	v_exp_f16_sdwa v51, v161 clamp dst_sel:WORD_1 dst_unused:UNUSED_PRESERVE src0_sel:WORD_1
	s_nop 0
	s_waitcnt lgkmcnt(5)
	v_mfma_f32_32x32x16_f16 v[34:49], v[114:117], v[58:61], v[34:49]
	ds_read_b128 v[248:251], v179 offset:34048
	v_pk_fma_f16 v51, v51, s55, v233 op_sel_hi:[1,0,0]
	v_pk_fma_f16 v50, v50, s55, v233 op_sel_hi:[1,0,0]
	v_pk_max_f16 v51, v161, v51
	v_pk_max_f16 v50, v160, v50
	s_waitcnt lgkmcnt(5)
	v_mfma_f32_32x32x16_f16 v[34:49], v[86:89], v[62:65], v[34:49]
	ds_read_b128 v[252:255], v179 offset:34080
	v_cvt_pk_f16_f32 v52, v22, v23
	v_cvt_pk_f16_f32 v53, v24, v25
	s_waitcnt lgkmcnt(5)
	v_mfma_f32_32x32x16_f16 v[34:49], v[126:129], v[166:169], v[34:49]
	ds_read_b128 v[22:25], v179 offset:34112
	v_exp_f16_e64 v54, v52 clamp
	v_exp_f16_e64 v55, v53 clamp
	v_exp_f16_sdwa v54, v52 clamp dst_sel:WORD_1 dst_unused:UNUSED_PRESERVE src0_sel:WORD_1
	v_exp_f16_sdwa v55, v53 clamp dst_sel:WORD_1 dst_unused:UNUSED_PRESERVE src0_sel:WORD_1
	s_nop 0
	s_waitcnt lgkmcnt(5)
	v_mfma_f32_32x32x16_f16 v[34:49], v[90:93], v[240:243], v[34:49]
	ds_read_b128 v[166:169], v179 offset:34144
	v_pk_fma_f16 v55, v55, s55, v233 op_sel_hi:[1,0,0]
	v_pk_fma_f16 v54, v54, s55, v233 op_sel_hi:[1,0,0]
	v_pk_max_f16 v53, v53, v55
	v_pk_max_f16 v52, v52, v54
	s_waitcnt lgkmcnt(5)
	v_mfma_f32_32x32x16_f16 v[34:49], v[118:121], v[244:247], v[34:49]
	ds_read_b128 v[240:243], v179 offset:34176
	v_cvt_pk_f16_f32 v160, v26, v27
	v_cvt_pk_f16_f32 v161, v28, v29
	v_mfma_f32_16x16x32_f16 v[62:65], v[70:73], v[50:53], 0
	s_waitcnt lgkmcnt(5)
	v_mfma_f32_32x32x16_f16 v[34:49], v[78:81], v[18:21], v[34:49]
	ds_read_b128 v[26:29], v179 offset:34208
	v_exp_f16_e64 v244, v160 clamp
	v_exp_f16_e64 v245, v161 clamp
	v_exp_f16_sdwa v244, v160 clamp dst_sel:WORD_1 dst_unused:UNUSED_PRESERVE src0_sel:WORD_1
	v_exp_f16_sdwa v245, v161 clamp dst_sel:WORD_1 dst_unused:UNUSED_PRESERVE src0_sel:WORD_1
	s_nop 0
	s_waitcnt lgkmcnt(5)
	v_mfma_f32_32x32x16_f16 v[34:49], v[102:105], v[248:251], v[34:49]
	ds_read_b128 v[18:21], v179 offset:34240
	v_pk_fma_f16 v245, v245, s55, v233 op_sel_hi:[1,0,0]
	s_nop 0
	v_pk_max_f16 v245, v161, v245
	v_pk_fma_f16 v161, v244, s55, v233 op_sel_hi:[1,0,0]
	s_nop 0
	v_pk_max_f16 v244, v160, v161
	s_waitcnt lgkmcnt(5)
	v_mfma_f32_32x32x16_f16 v[34:49], v[74:77], v[252:255], v[34:49]
	ds_read_b128 v[248:251], v179 offset:34272
	v_cvt_pk_f16_f32 v30, v30, v31
	v_cvt_pk_f16_f32 v31, v32, v33
	s_waitcnt lgkmcnt(5)
	v_mfma_f32_32x32x16_f16 v[34:49], v[106:109], v[22:25], v[34:49]
	v_exp_f16_e64 v32, v30 clamp
	v_exp_f16_e64 v33, v31 clamp
	v_exp_f16_sdwa v32, v30 clamp dst_sel:WORD_1 dst_unused:UNUSED_PRESERVE src0_sel:WORD_1
	v_exp_f16_sdwa v33, v31 clamp dst_sel:WORD_1 dst_unused:UNUSED_PRESERVE src0_sel:WORD_1
	s_nop 0
	s_waitcnt lgkmcnt(4)
	v_mfma_f32_32x32x16_f16 v[34:49], v[82:85], v[166:169], v[34:49]
	v_pk_fma_f16 v22, v33, s55, v233 op_sel_hi:[1,0,0]
	s_nop 0
	v_pk_max_f16 v247, v31, v22
	v_pk_fma_f16 v22, v32, s55, v233 op_sel_hi:[1,0,0]
	s_nop 0
	v_pk_max_f16 v246, v30, v22
	s_waitcnt lgkmcnt(3)
	v_mfma_f32_32x32x16_f16 v[34:49], v[110:113], v[240:243], v[34:49]
	s_waitcnt vmcnt(2)
	v_pk_add_f16 v24, v146, v162
	v_pk_add_f16 v25, v147, v163
	s_nop 0
	v_pk_mul_f16 v22, v164, v148 clamp
	v_pk_mul_f16 v23, v165, v149 clamp
	v_pk_max_f16 v22, v24, v22
	v_pk_max_f16 v23, v25, v23
	ds_write_b64 v189, v[22:23]
	v_mfma_f32_16x16x32_f16 v[62:65], v[66:69], v[244:247], v[62:65]
	s_waitcnt lgkmcnt(3)
	v_mfma_f32_32x32x16_f16 v[34:49], v[94:97], v[26:29], v[34:49]
	v_pk_add_f16 v24, v138, v162
	v_pk_add_f16 v25, v139, v163
	s_nop 0
	v_pk_mul_f16 v22, v164, v140 clamp
	v_pk_mul_f16 v23, v165, v141 clamp
	v_pk_max_f16 v22, v24, v22
	v_pk_max_f16 v23, v25, v23
	ds_write_b64 v189, v[22:23] offset:528
	s_waitcnt lgkmcnt(3)
	v_mfma_f32_32x32x16_f16 v[34:49], v[134:137], v[18:21], v[34:49]
	v_pk_add_f16 v24, v150, v162
	v_pk_add_f16 v25, v151, v163
	s_nop 0
	v_pk_mul_f16 v22, v164, v152 clamp
	v_pk_mul_f16 v23, v165, v153 clamp
	v_pk_max_f16 v22, v24, v22
	v_pk_max_f16 v23, v25, v23
	ds_write_b64 v189, v[22:23] offset:1056
	s_waitcnt lgkmcnt(3)
	v_mfma_f32_32x32x16_f16 v[34:49], v[130:133], v[248:251], v[34:49]
	s_waitcnt vmcnt(1)
	v_pk_add_f16 v20, v142, v162
	v_pk_add_f16 v21, v143, v163
	s_nop 0
	v_pk_mul_f16 v18, v164, v144 clamp
	v_pk_mul_f16 v19, v165, v145 clamp
	v_pk_max_f16 v18, v20, v18
	v_pk_max_f16 v19, v21, v19
	ds_write_b64 v189, v[18:19] offset:1584
	ds_write2_b32 v201, v62, v63 offset1:1
	s_and_saveexec_b64 s[30:31], s[0:1]
	ds_write2_b32 v201, v64, v65 offset0:2 offset1:3
	s_or_b64 exec, exec, s[30:31]
	v_lshl_add_u64 v[158:159], s[20:21], 4, v[158:159]
	global_load_dwordx4 v[166:169], v[158:159], off
	ds_read_b128 v[50:53], v179 offset:50688
	ds_read_b128 v[54:57], v179 offset:50720
	ds_read_b128 v[58:61], v179 offset:50752
	ds_read_b128 v[62:65], v179 offset:50784
	ds_read_b128 v[160:163], v179 offset:50816
	ds_read_b128 v[240:243], v179 offset:50848
	s_waitcnt lgkmcnt(5)
	v_mfma_f32_32x32x16_f16 v[18:33], v[122:125], v[50:53], v[2:17]
	ds_read_b128 v[244:247], v179 offset:50880
	v_cvt_pk_f16_f32 v164, v34, v35
	v_cvt_pk_f16_f32 v165, v36, v37
	s_waitcnt lgkmcnt(5)
	v_mfma_f32_32x32x16_f16 v[18:33], v[98:101], v[54:57], v[18:33]
	ds_read_b128 v[34:37], v179 offset:50912
	v_exp_f16_e64 v50, v164 clamp
	v_exp_f16_e64 v51, v165 clamp
	v_exp_f16_sdwa v50, v164 clamp dst_sel:WORD_1 dst_unused:UNUSED_PRESERVE src0_sel:WORD_1
	v_exp_f16_sdwa v51, v165 clamp dst_sel:WORD_1 dst_unused:UNUSED_PRESERVE src0_sel:WORD_1
	s_nop 0
	s_waitcnt lgkmcnt(5)
	v_mfma_f32_32x32x16_f16 v[18:33], v[114:117], v[58:61], v[18:33]
	ds_read_b128 v[248:251], v179 offset:50944
	v_pk_fma_f16 v51, v51, s55, v233 op_sel_hi:[1,0,0]
	v_pk_fma_f16 v50, v50, s55, v233 op_sel_hi:[1,0,0]
	v_pk_max_f16 v51, v165, v51
	v_pk_max_f16 v50, v164, v50
	s_waitcnt lgkmcnt(5)
	v_mfma_f32_32x32x16_f16 v[18:33], v[86:89], v[62:65], v[18:33]
	ds_read_b128 v[252:255], v179 offset:50976
	v_cvt_pk_f16_f32 v52, v38, v39
	v_cvt_pk_f16_f32 v53, v40, v41
	s_waitcnt lgkmcnt(5)
	v_mfma_f32_32x32x16_f16 v[18:33], v[126:129], v[160:163], v[18:33]
	ds_read_b128 v[38:41], v179 offset:51008
	v_exp_f16_e64 v54, v52 clamp
	v_exp_f16_e64 v55, v53 clamp
	v_exp_f16_sdwa v54, v52 clamp dst_sel:WORD_1 dst_unused:UNUSED_PRESERVE src0_sel:WORD_1
	v_exp_f16_sdwa v55, v53 clamp dst_sel:WORD_1 dst_unused:UNUSED_PRESERVE src0_sel:WORD_1
	s_nop 0
	s_waitcnt lgkmcnt(5)
	v_mfma_f32_32x32x16_f16 v[18:33], v[90:93], v[240:243], v[18:33]
	ds_read_b128 v[160:163], v179 offset:51040
	v_pk_fma_f16 v55, v55, s55, v233 op_sel_hi:[1,0,0]
	v_pk_fma_f16 v54, v54, s55, v233 op_sel_hi:[1,0,0]
	v_pk_max_f16 v53, v53, v55
	v_pk_max_f16 v52, v52, v54
	s_waitcnt lgkmcnt(5)
	v_mfma_f32_32x32x16_f16 v[18:33], v[118:121], v[244:247], v[18:33]
	ds_read_b128 v[240:243], v179 offset:51072
	v_cvt_pk_f16_f32 v164, v42, v43
	v_cvt_pk_f16_f32 v165, v44, v45
	v_mfma_f32_16x16x32_f16 v[62:65], v[70:73], v[50:53], 0
	s_waitcnt lgkmcnt(5)
	v_mfma_f32_32x32x16_f16 v[18:33], v[78:81], v[34:37], v[18:33]
	ds_read_b128 v[42:45], v179 offset:51104
	v_exp_f16_e64 v244, v164 clamp
	v_exp_f16_e64 v245, v165 clamp
	v_exp_f16_sdwa v244, v164 clamp dst_sel:WORD_1 dst_unused:UNUSED_PRESERVE src0_sel:WORD_1
	v_exp_f16_sdwa v245, v165 clamp dst_sel:WORD_1 dst_unused:UNUSED_PRESERVE src0_sel:WORD_1
	s_nop 0
	s_waitcnt lgkmcnt(5)
	v_mfma_f32_32x32x16_f16 v[18:33], v[102:105], v[248:251], v[18:33]
	ds_read_b128 v[34:37], v179 offset:51136
	v_pk_fma_f16 v245, v245, s55, v233 op_sel_hi:[1,0,0]
	s_nop 0
	v_pk_max_f16 v245, v165, v245
	v_pk_fma_f16 v165, v244, s55, v233 op_sel_hi:[1,0,0]
	s_nop 0
	v_pk_max_f16 v244, v164, v165
	s_waitcnt lgkmcnt(5)
	v_mfma_f32_32x32x16_f16 v[18:33], v[74:77], v[252:255], v[18:33]
	ds_read_b128 v[248:251], v179 offset:51168
	v_cvt_pk_f16_f32 v46, v46, v47
	v_cvt_pk_f16_f32 v47, v48, v49
	s_waitcnt lgkmcnt(5)
	v_mfma_f32_32x32x16_f16 v[18:33], v[106:109], v[38:41], v[18:33]
	v_exp_f16_e64 v48, v46 clamp
	v_exp_f16_e64 v49, v47 clamp
	v_exp_f16_sdwa v48, v46 clamp dst_sel:WORD_1 dst_unused:UNUSED_PRESERVE src0_sel:WORD_1
	v_exp_f16_sdwa v49, v47 clamp dst_sel:WORD_1 dst_unused:UNUSED_PRESERVE src0_sel:WORD_1
	s_nop 0
	s_waitcnt lgkmcnt(4)
	v_mfma_f32_32x32x16_f16 v[18:33], v[82:85], v[160:163], v[18:33]
	v_pk_fma_f16 v38, v49, s55, v233 op_sel_hi:[1,0,0]
	s_nop 0
	v_pk_max_f16 v247, v47, v38
	v_pk_fma_f16 v38, v48, s55, v233 op_sel_hi:[1,0,0]
	s_nop 0
	v_pk_max_f16 v246, v46, v38
	s_waitcnt lgkmcnt(3)
	v_mfma_f32_32x32x16_f16 v[18:33], v[110:113], v[240:243], v[18:33]
	v_pk_add_f16 v40, v146, v154
	v_pk_add_f16 v41, v147, v155
	s_nop 0
	v_pk_mul_f16 v38, v156, v148 clamp
	v_pk_mul_f16 v39, v157, v149 clamp
	v_pk_max_f16 v38, v40, v38
	v_pk_max_f16 v39, v41, v39
	ds_write_b64 v189, v[38:39] offset:16896
	v_mfma_f32_16x16x32_f16 v[62:65], v[66:69], v[244:247], v[62:65]
	s_waitcnt lgkmcnt(3)
	v_mfma_f32_32x32x16_f16 v[18:33], v[94:97], v[42:45], v[18:33]
	v_pk_add_f16 v40, v138, v154
	v_pk_add_f16 v41, v139, v155
	s_nop 0
	v_pk_mul_f16 v38, v156, v140 clamp
	v_pk_mul_f16 v39, v157, v141 clamp
	v_pk_max_f16 v38, v40, v38
	v_pk_max_f16 v39, v41, v39
	ds_write_b64 v189, v[38:39] offset:17424
	s_waitcnt lgkmcnt(3)
	v_mfma_f32_32x32x16_f16 v[18:33], v[134:137], v[34:37], v[18:33]
	v_pk_add_f16 v40, v150, v154
	v_pk_add_f16 v41, v151, v155
	s_nop 0
	v_pk_mul_f16 v38, v156, v152 clamp
	v_pk_mul_f16 v39, v157, v153 clamp
	v_pk_max_f16 v38, v40, v38
	v_pk_max_f16 v39, v41, v39
	ds_write_b64 v189, v[38:39] offset:17952
	s_waitcnt lgkmcnt(3)
	v_mfma_f32_32x32x16_f16 v[18:33], v[130:133], v[248:251], v[18:33]
	v_pk_add_f16 v36, v142, v154
	v_pk_add_f16 v37, v143, v155
	s_nop 0
	v_pk_mul_f16 v34, v156, v144 clamp
	v_pk_mul_f16 v35, v157, v145 clamp
	v_pk_max_f16 v34, v36, v34
	v_pk_max_f16 v35, v37, v35
	ds_write_b64 v189, v[34:35] offset:18480
	ds_write2_b32 v211, v62, v63 offset1:1
	s_and_saveexec_b64 s[30:31], s[0:1]
	ds_write2_b32 v211, v64, v65 offset0:2 offset1:3
	s_or_b64 exec, exec, s[30:31]
	s_sub_i32 s30, 0x7d, s34
	s_mul_i32 s30, s30, 6
	s_ashr_i32 s31, s30, 31
	s_add_u32 s28, s28, s30
	s_addc_u32 s29, s29, s31
	s_and_b64 vcc, exec, s[8:9]
	s_waitcnt lgkmcnt(0)
	s_barrier
	ds_read_b128 v[50:53], v179
	s_cbranch_vccnz .LBB1_110
	s_cmp_eq_u32 s41, 0
	s_cbranch_scc1 .LBB1_106
	s_and_saveexec_b64 s[30:31], s[6:7]
	s_cbranch_execz .LBB1_105
	ds_read2_b32 v[34:35], v200 offset1:224
	ds_read2_b32 v[36:37], v234 offset1:224
	ds_read2_b32 v[38:39], v235 offset1:224
	ds_read2_b32 v[40:41], v236 offset1:224
	s_lshl_b32 s35, s56, 28
	s_add_i32 s35, s35, 0xd0000000
	s_ashr_i32 s35, s35, 31
	s_waitcnt lgkmcnt(3)
	v_add_f32_e32 v34, 0, v34
	v_add_f32_e32 v34, v34, v35
	s_waitcnt lgkmcnt(2)
	v_add_f32_e32 v34, v34, v36
	v_add_f32_e32 v34, v34, v37
	s_waitcnt lgkmcnt(1)
	v_add_f32_e32 v34, v34, v38
	v_add_f32_e32 v34, v34, v39
	s_waitcnt lgkmcnt(0)
	v_add_f32_e32 v34, v34, v40
	s_and_b32 s35, s35, 0x1800
	v_add_f32_e32 v34, v34, v41
	v_add_u32_e32 v35, s35, v232
	ds_write_b32 v35, v34 offset:640

.LBB1_119:
	v_lshl_add_u64 v[154:155], s[20:21], 4, v[158:159]
	global_load_dwordx4 v[158:161], v[154:155], off
	ds_read_b128 v[54:57], v179 offset:32
	ds_read_b128 v[58:61], v179 offset:64
	ds_read_b128 v[62:65], v179 offset:96
	ds_read_b128 v[162:165], v179 offset:128
	ds_read_b128 v[240:243], v179 offset:160
	s_waitcnt lgkmcnt(5)
	v_mfma_f32_32x32x16_f16 v[34:49], v[122:125], v[50:53], v[2:17]
	ds_read_b128 v[244:247], v179 offset:192
	v_cvt_pk_f16_f32 v156, v18, v19
	v_cvt_pk_f16_f32 v157, v20, v21
	s_waitcnt lgkmcnt(5)
	v_mfma_f32_32x32x16_f16 v[34:49], v[98:101], v[54:57], v[34:49]
	ds_read_b128 v[18:21], v179 offset:224
	v_exp_f16_e64 v50, v156 clamp
	v_exp_f16_e64 v51, v157 clamp
	v_exp_f16_sdwa v50, v156 clamp dst_sel:WORD_1 dst_unused:UNUSED_PRESERVE src0_sel:WORD_1
	v_exp_f16_sdwa v51, v157 clamp dst_sel:WORD_1 dst_unused:UNUSED_PRESERVE src0_sel:WORD_1
	s_nop 0
	s_waitcnt lgkmcnt(5)
	v_mfma_f32_32x32x16_f16 v[34:49], v[114:117], v[58:61], v[34:49]
	ds_read_b128 v[248:251], v179 offset:256
	v_pk_fma_f16 v51, v51, s55, v233 op_sel_hi:[1,0,0]
	v_pk_fma_f16 v50, v50, s55, v233 op_sel_hi:[1,0,0]
	v_pk_max_f16 v51, v157, v51
	v_pk_max_f16 v50, v156, v50
	s_waitcnt lgkmcnt(5)
	v_mfma_f32_32x32x16_f16 v[34:49], v[86:89], v[62:65], v[34:49]
	ds_read_b128 v[252:255], v179 offset:288
	v_cvt_pk_f16_f32 v52, v22, v23
	v_cvt_pk_f16_f32 v53, v24, v25
	s_waitcnt lgkmcnt(5)
	v_mfma_f32_32x32x16_f16 v[34:49], v[126:129], v[162:165], v[34:49]
	ds_read_b128 v[22:25], v179 offset:320
	v_exp_f16_e64 v54, v52 clamp
	v_exp_f16_e64 v55, v53 clamp
	v_exp_f16_sdwa v54, v52 clamp dst_sel:WORD_1 dst_unused:UNUSED_PRESERVE src0_sel:WORD_1
	v_exp_f16_sdwa v55, v53 clamp dst_sel:WORD_1 dst_unused:UNUSED_PRESERVE src0_sel:WORD_1
	s_nop 0
	s_waitcnt lgkmcnt(5)
	v_mfma_f32_32x32x16_f16 v[34:49], v[90:93], v[240:243], v[34:49]
	ds_read_b128 v[162:165], v179 offset:352
	v_pk_fma_f16 v55, v55, s55, v233 op_sel_hi:[1,0,0]
	v_pk_fma_f16 v54, v54, s55, v233 op_sel_hi:[1,0,0]
	v_pk_max_f16 v53, v53, v55
	v_pk_max_f16 v52, v52, v54
	s_waitcnt lgkmcnt(5)
	v_mfma_f32_32x32x16_f16 v[34:49], v[118:121], v[244:247], v[34:49]
	ds_read_b128 v[240:243], v179 offset:384
	v_cvt_pk_f16_f32 v156, v26, v27
	v_cvt_pk_f16_f32 v157, v28, v29
	v_mfma_f32_16x16x32_f16 v[62:65], v[70:73], v[50:53], 0
	s_waitcnt lgkmcnt(5)
	v_mfma_f32_32x32x16_f16 v[34:49], v[78:81], v[18:21], v[34:49]
	ds_read_b128 v[26:29], v179 offset:416
	v_exp_f16_e64 v244, v156 clamp
	v_exp_f16_e64 v245, v157 clamp
	v_exp_f16_sdwa v244, v156 clamp dst_sel:WORD_1 dst_unused:UNUSED_PRESERVE src0_sel:WORD_1
	v_exp_f16_sdwa v245, v157 clamp dst_sel:WORD_1 dst_unused:UNUSED_PRESERVE src0_sel:WORD_1
	s_nop 0
	s_waitcnt lgkmcnt(5)
	v_mfma_f32_32x32x16_f16 v[34:49], v[102:105], v[248:251], v[34:49]
	ds_read_b128 v[18:21], v179 offset:448
	v_pk_fma_f16 v245, v245, s55, v233 op_sel_hi:[1,0,0]
	s_nop 0
	v_pk_max_f16 v245, v157, v245
	v_pk_fma_f16 v157, v244, s55, v233 op_sel_hi:[1,0,0]
	s_nop 0
	v_pk_max_f16 v244, v156, v157
	s_waitcnt lgkmcnt(5)
	v_mfma_f32_32x32x16_f16 v[34:49], v[74:77], v[252:255], v[34:49]
	ds_read_b128 v[248:251], v179 offset:480
	v_cvt_pk_f16_f32 v30, v30, v31
	v_cvt_pk_f16_f32 v31, v32, v33
	s_waitcnt lgkmcnt(5)
	v_mfma_f32_32x32x16_f16 v[34:49], v[106:109], v[22:25], v[34:49]
	v_exp_f16_e64 v32, v30 clamp
	v_exp_f16_e64 v33, v31 clamp
	v_exp_f16_sdwa v32, v30 clamp dst_sel:WORD_1 dst_unused:UNUSED_PRESERVE src0_sel:WORD_1
	v_exp_f16_sdwa v33, v31 clamp dst_sel:WORD_1 dst_unused:UNUSED_PRESERVE src0_sel:WORD_1
	s_nop 0
	s_waitcnt lgkmcnt(4)
	v_mfma_f32_32x32x16_f16 v[34:49], v[82:85], v[162:165], v[34:49]
	v_pk_fma_f16 v22, v33, s55, v233 op_sel_hi:[1,0,0]
	s_nop 0
	v_pk_max_f16 v247, v31, v22
	v_pk_fma_f16 v22, v32, s55, v233 op_sel_hi:[1,0,0]
	s_nop 0
	v_pk_max_f16 v246, v30, v22
	s_waitcnt lgkmcnt(3)
	v_mfma_f32_32x32x16_f16 v[34:49], v[110:113], v[240:243], v[34:49]
	s_waitcnt vmcnt(2)
	v_pk_add_f16 v24, v170, v146
	v_pk_add_f16 v25, v171, v147
	s_nop 0
	v_pk_mul_f16 v22, v172, v148 clamp
	v_pk_mul_f16 v23, v173, v149 clamp
	v_pk_max_f16 v22, v24, v22
	v_pk_max_f16 v23, v25, v23
	ds_write_b64 v189, v[22:23] offset:33792
	v_mfma_f32_16x16x32_f16 v[62:65], v[66:69], v[244:247], v[62:65]
	s_waitcnt lgkmcnt(3)
	v_mfma_f32_32x32x16_f16 v[34:49], v[94:97], v[26:29], v[34:49]
	v_pk_add_f16 v24, v170, v138
	v_pk_add_f16 v25, v171, v139
	s_nop 0
	v_pk_mul_f16 v22, v172, v140 clamp
	v_pk_mul_f16 v23, v173, v141 clamp
	v_pk_max_f16 v22, v24, v22
	v_pk_max_f16 v23, v25, v23
	ds_write_b64 v189, v[22:23] offset:34320
	s_waitcnt lgkmcnt(3)
	v_mfma_f32_32x32x16_f16 v[34:49], v[134:137], v[18:21], v[34:49]
	v_pk_add_f16 v24, v170, v150
	v_pk_add_f16 v25, v171, v151
	s_nop 0
	v_pk_mul_f16 v22, v172, v152 clamp
	v_pk_mul_f16 v23, v173, v153 clamp
	v_pk_max_f16 v22, v24, v22
	v_pk_max_f16 v23, v25, v23
	ds_write_b64 v189, v[22:23] offset:34848
	s_waitcnt lgkmcnt(3)
	v_mfma_f32_32x32x16_f16 v[34:49], v[130:133], v[248:251], v[34:49]
	v_pk_add_f16 v20, v170, v142
	v_pk_add_f16 v21, v171, v143
	s_nop 0
	v_pk_mul_f16 v18, v172, v144 clamp
	v_pk_mul_f16 v19, v173, v145 clamp
	v_pk_max_f16 v18, v20, v18
	v_pk_max_f16 v19, v21, v19
	ds_write_b64 v189, v[18:19] offset:35376
	ds_write2_b32 v229, v62, v63 offset1:1
	s_and_saveexec_b64 s[30:31], s[0:1]
	ds_write2_b32 v229, v64, v65 offset0:2 offset1:3
	s_or_b64 exec, exec, s[30:31]
	s_cmp_eq_u32 s56, 16
	s_cbranch_scc0 .Lw2_sw_skip
	s_and_b64 vcc, exec, s[16:17]
	s_cbranch_vccz .Lw2_sw_skip
	v_mov_b32_dpp v70, v70 row_shl:8 row_mask:0xa bank_mask:0x3
	v_mov_b32_dpp v71, v71 row_shl:8 row_mask:0xa bank_mask:0x3
	v_mov_b32_dpp v72, v72 row_shl:8 row_mask:0xa bank_mask:0x3
	v_mov_b32_dpp v73, v73 row_shl:8 row_mask:0xa bank_mask:0x3
	v_mov_b32_dpp v66, v66 row_shl:8 row_mask:0xa bank_mask:0x3
	v_mov_b32_dpp v67, v67 row_shl:8 row_mask:0xa bank_mask:0x3
	v_mov_b32_dpp v68, v68 row_shl:8 row_mask:0xa bank_mask:0x3
	v_mov_b32_dpp v69, v69 row_shl:8 row_mask:0xa bank_mask:0x3
.Lw2_sw_skip:
	v_lshl_add_u64 v[154:155], s[20:21], 4, v[154:155]
	global_load_dwordx4 v[162:165], v[154:155], off
	ds_read_b128 v[50:53], v179 offset:16896
	ds_read_b128 v[54:57], v179 offset:16928
	ds_read_b128 v[58:61], v179 offset:16960
	ds_read_b128 v[62:65], v179 offset:16992
	ds_read_b128 v[170:173], v179 offset:17024
	ds_read_b128 v[240:243], v179 offset:17056
	s_waitcnt lgkmcnt(5)
	v_mfma_f32_32x32x16_f16 v[18:33], v[122:125], v[50:53], v[2:17]
	ds_read_b128 v[244:247], v179 offset:17088
	v_cvt_pk_f16_f32 v156, v34, v35
	v_cvt_pk_f16_f32 v157, v36, v37
	s_waitcnt lgkmcnt(5)
	v_mfma_f32_32x32x16_f16 v[18:33], v[98:101], v[54:57], v[18:33]
	ds_read_b128 v[34:37], v179 offset:17120
	v_exp_f16_e64 v50, v156 clamp
	v_exp_f16_e64 v51, v157 clamp
	v_exp_f16_sdwa v50, v156 clamp dst_sel:WORD_1 dst_unused:UNUSED_PRESERVE src0_sel:WORD_1
	v_exp_f16_sdwa v51, v157 clamp dst_sel:WORD_1 dst_unused:UNUSED_PRESERVE src0_sel:WORD_1
	s_nop 0
	s_waitcnt lgkmcnt(5)
	v_mfma_f32_32x32x16_f16 v[18:33], v[114:117], v[58:61], v[18:33]
	ds_read_b128 v[248:251], v179 offset:17152
	v_pk_fma_f16 v51, v51, s55, v233 op_sel_hi:[1,0,0]
	v_pk_fma_f16 v50, v50, s55, v233 op_sel_hi:[1,0,0]
	v_pk_max_f16 v51, v157, v51
	v_pk_max_f16 v50, v156, v50
	s_waitcnt lgkmcnt(5)
	v_mfma_f32_32x32x16_f16 v[18:33], v[86:89], v[62:65], v[18:33]
	ds_read_b128 v[252:255], v179 offset:17184
	v_cvt_pk_f16_f32 v52, v38, v39
	v_cvt_pk_f16_f32 v53, v40, v41
	s_waitcnt lgkmcnt(5)
	v_mfma_f32_32x32x16_f16 v[18:33], v[126:129], v[170:173], v[18:33]
	ds_read_b128 v[38:41], v179 offset:17216
	v_exp_f16_e64 v54, v52 clamp
	v_exp_f16_e64 v55, v53 clamp
	v_exp_f16_sdwa v54, v52 clamp dst_sel:WORD_1 dst_unused:UNUSED_PRESERVE src0_sel:WORD_1
	v_exp_f16_sdwa v55, v53 clamp dst_sel:WORD_1 dst_unused:UNUSED_PRESERVE src0_sel:WORD_1
	s_nop 0
	s_waitcnt lgkmcnt(5)
	v_mfma_f32_32x32x16_f16 v[18:33], v[90:93], v[240:243], v[18:33]
	ds_read_b128 v[170:173], v179 offset:17248
	v_pk_fma_f16 v55, v55, s55, v233 op_sel_hi:[1,0,0]
	v_pk_fma_f16 v54, v54, s55, v233 op_sel_hi:[1,0,0]
	v_pk_max_f16 v53, v53, v55
	v_pk_max_f16 v52, v52, v54
	s_waitcnt lgkmcnt(5)
	v_mfma_f32_32x32x16_f16 v[18:33], v[118:121], v[244:247], v[18:33]
	ds_read_b128 v[240:243], v179 offset:17280
	v_cvt_pk_f16_f32 v156, v42, v43
	v_cvt_pk_f16_f32 v157, v44, v45
	v_mfma_f32_16x16x32_f16 v[62:65], v[70:73], v[50:53], 0
	s_waitcnt lgkmcnt(5)
	v_mfma_f32_32x32x16_f16 v[18:33], v[78:81], v[34:37], v[18:33]
	ds_read_b128 v[42:45], v179 offset:17312
	v_exp_f16_e64 v244, v156 clamp
	v_exp_f16_e64 v245, v157 clamp
	v_exp_f16_sdwa v244, v156 clamp dst_sel:WORD_1 dst_unused:UNUSED_PRESERVE src0_sel:WORD_1
	v_exp_f16_sdwa v245, v157 clamp dst_sel:WORD_1 dst_unused:UNUSED_PRESERVE src0_sel:WORD_1
	s_nop 0
	s_waitcnt lgkmcnt(5)
	v_mfma_f32_32x32x16_f16 v[18:33], v[102:105], v[248:251], v[18:33]
	ds_read_b128 v[34:37], v179 offset:17344
	v_pk_fma_f16 v245, v245, s55, v233 op_sel_hi:[1,0,0]
	s_nop 0
	v_pk_max_f16 v245, v157, v245
	v_pk_fma_f16 v157, v244, s55, v233 op_sel_hi:[1,0,0]
	s_nop 0
	v_pk_max_f16 v244, v156, v157
	s_waitcnt lgkmcnt(5)
	v_mfma_f32_32x32x16_f16 v[18:33], v[74:77], v[252:255], v[18:33]
	ds_read_b128 v[248:251], v179 offset:17376
	v_cvt_pk_f16_f32 v46, v46, v47
	v_cvt_pk_f16_f32 v47, v48, v49
	s_waitcnt lgkmcnt(5)
	v_mfma_f32_32x32x16_f16 v[18:33], v[106:109], v[38:41], v[18:33]
	v_exp_f16_e64 v48, v46 clamp
	v_exp_f16_e64 v49, v47 clamp
	v_exp_f16_sdwa v48, v46 clamp dst_sel:WORD_1 dst_unused:UNUSED_PRESERVE src0_sel:WORD_1
	v_exp_f16_sdwa v49, v47 clamp dst_sel:WORD_1 dst_unused:UNUSED_PRESERVE src0_sel:WORD_1
	s_nop 0
	s_waitcnt lgkmcnt(4)
	v_mfma_f32_32x32x16_f16 v[18:33], v[82:85], v[170:173], v[18:33]
	v_pk_fma_f16 v38, v49, s55, v233 op_sel_hi:[1,0,0]
	s_nop 0
	v_pk_max_f16 v247, v47, v38
	v_pk_fma_f16 v38, v48, s55, v233 op_sel_hi:[1,0,0]
	s_nop 0
	v_pk_max_f16 v246, v46, v38
	s_waitcnt lgkmcnt(3)
	v_mfma_f32_32x32x16_f16 v[18:33], v[110:113], v[240:243], v[18:33]
	s_waitcnt vmcnt(2)
	v_pk_add_f16 v40, v166, v146
	v_pk_add_f16 v41, v167, v147
	s_nop 0
	v_pk_mul_f16 v38, v168, v148 clamp
	v_pk_mul_f16 v39, v169, v149 clamp
	v_pk_max_f16 v38, v40, v38
	v_pk_max_f16 v39, v41, v39
	ds_write_b64 v189, v[38:39] offset:50688
	v_mfma_f32_16x16x32_f16 v[62:65], v[66:69], v[244:247], v[62:65]
	s_waitcnt lgkmcnt(3)
	v_mfma_f32_32x32x16_f16 v[18:33], v[94:97], v[42:45], v[18:33]
	v_pk_add_f16 v40, v166, v138
	v_pk_add_f16 v41, v167, v139
	s_nop 0
	v_pk_mul_f16 v38, v168, v140 clamp
	v_pk_mul_f16 v39, v169, v141 clamp
	v_pk_max_f16 v38, v40, v38
	v_pk_max_f16 v39, v41, v39
	ds_write_b64 v189, v[38:39] offset:51216
	s_waitcnt lgkmcnt(3)
	v_mfma_f32_32x32x16_f16 v[18:33], v[134:137], v[34:37], v[18:33]
	v_pk_add_f16 v40, v166, v150
	v_pk_add_f16 v41, v167, v151
	s_nop 0
	v_pk_mul_f16 v38, v168, v152 clamp
	v_pk_mul_f16 v39, v169, v153 clamp
	v_pk_max_f16 v38, v40, v38
	v_pk_max_f16 v39, v41, v39
	ds_write_b64 v189, v[38:39] offset:51744
	s_waitcnt lgkmcnt(3)
	v_mfma_f32_32x32x16_f16 v[18:33], v[130:133], v[248:251], v[18:33]
	v_pk_add_f16 v36, v166, v142
	v_pk_add_f16 v37, v167, v143
	s_nop 0
	v_pk_mul_f16 v34, v168, v144 clamp
	v_pk_mul_f16 v35, v169, v145 clamp
	v_pk_max_f16 v34, v36, v34
	v_pk_max_f16 v35, v37, v35
	ds_write_b64 v189, v[34:35] offset:52272
	ds_write2_b32 v206, v62, v63 offset1:1
	s_and_saveexec_b64 s[30:31], s[0:1]
	ds_write2_b32 v206, v64, v65 offset0:2 offset1:3
	s_or_b64 exec, exec, s[30:31]
	s_add_i32 s34, s34, 1
	s_sub_i32 s30, 0x7d, s34
	s_mul_i32 s30, s30, 6
	s_ashr_i32 s31, s30, 31
	s_add_u32 s28, s28, s30
	s_addc_u32 s29, s29, s31
	s_and_b64 vcc, exec, s[8:9]
	s_waitcnt lgkmcnt(0)
	s_barrier
	ds_read_b128 v[50:53], v179 offset:33792
	s_cbranch_vccnz .LBB1_136
	s_cmp_eq_u32 s41, 0
	s_cbranch_scc1 .LBB1_132
	s_and_saveexec_b64 s[30:31], s[6:7]
	s_cbranch_execz .LBB1_131
	ds_read2_b32 v[34:35], v180 offset1:224
	v_add_u32_e32 v36, 0x700, v180
	ds_read2_b32 v[36:37], v36 offset1:224
	v_add_u32_e32 v38, 0xe00, v180
	s_lshl_b32 s35, s56, 28
	s_waitcnt lgkmcnt(1)
	v_add_f32_e32 v34, 0, v34
	v_add_f32_e32 v40, v34, v35
	ds_read2_b32 v[34:35], v38 offset1:224
	v_add_u32_e32 v38, 0x1500, v180
	ds_read2_b32 v[38:39], v38 offset1:224
	s_waitcnt lgkmcnt(2)
	v_add_f32_e32 v36, v40, v36
	v_add_f32_e32 v36, v36, v37
	s_waitcnt lgkmcnt(1)
	v_add_f32_e32 v34, v36, v34
	s_add_i32 s35, s35, 0xf0000000
	v_add_f32_e32 v34, v34, v35
	s_ashr_i32 s35, s35, 31
	s_waitcnt lgkmcnt(0)
	v_add_f32_e32 v34, v34, v38
	s_and_b32 s35, s35, 0x1800
	v_add_f32_e32 v34, v34, v39
	v_add_u32_e32 v35, s35, v232
	ds_write_b32 v35, v34 offset:896

.LBB1_145:
	v_lshl_add_u64 v[166:167], s[20:21], 4, v[154:155]
	global_load_dwordx4 v[154:157], v[166:167], off
	ds_read_b128 v[54:57], v179 offset:33824
	ds_read_b128 v[58:61], v179 offset:33856
	ds_read_b128 v[62:65], v179 offset:33888
	ds_read_b128 v[168:171], v179 offset:33920
	ds_read_b128 v[240:243], v179 offset:33952
	s_waitcnt lgkmcnt(5)
	v_mfma_f32_32x32x16_f16 v[34:49], v[122:125], v[50:53], v[2:17]
	ds_read_b128 v[244:247], v179 offset:33984
	v_cvt_pk_f16_f32 v172, v18, v19
	v_cvt_pk_f16_f32 v173, v20, v21
	s_waitcnt lgkmcnt(5)
	v_mfma_f32_32x32x16_f16 v[34:49], v[98:101], v[54:57], v[34:49]
	ds_read_b128 v[18:21], v179 offset:34016
	v_exp_f16_e64 v50, v172 clamp
	v_exp_f16_e64 v51, v173 clamp
	v_exp_f16_sdwa v50, v172 clamp dst_sel:WORD_1 dst_unused:UNUSED_PRESERVE src0_sel:WORD_1
	v_exp_f16_sdwa v51, v173 clamp dst_sel:WORD_1 dst_unused:UNUSED_PRESERVE src0_sel:WORD_1
	s_nop 0
	s_waitcnt lgkmcnt(5)
	v_mfma_f32_32x32x16_f16 v[34:49], v[114:117], v[58:61], v[34:49]
	ds_read_b128 v[248:251], v179 offset:34048
	v_pk_fma_f16 v51, v51, s55, v233 op_sel_hi:[1,0,0]
	v_pk_fma_f16 v50, v50, s55, v233 op_sel_hi:[1,0,0]
	v_pk_max_f16 v51, v173, v51
	v_pk_max_f16 v50, v172, v50
	s_waitcnt lgkmcnt(5)
	v_mfma_f32_32x32x16_f16 v[34:49], v[86:89], v[62:65], v[34:49]
	ds_read_b128 v[252:255], v179 offset:34080
	v_cvt_pk_f16_f32 v52, v22, v23
	v_cvt_pk_f16_f32 v53, v24, v25
	s_waitcnt lgkmcnt(5)
	v_mfma_f32_32x32x16_f16 v[34:49], v[126:129], v[168:171], v[34:49]
	ds_read_b128 v[22:25], v179 offset:34112
	v_exp_f16_e64 v54, v52 clamp
	v_exp_f16_e64 v55, v53 clamp
	v_exp_f16_sdwa v54, v52 clamp dst_sel:WORD_1 dst_unused:UNUSED_PRESERVE src0_sel:WORD_1
	v_exp_f16_sdwa v55, v53 clamp dst_sel:WORD_1 dst_unused:UNUSED_PRESERVE src0_sel:WORD_1
	s_nop 0
	s_waitcnt lgkmcnt(5)
	v_mfma_f32_32x32x16_f16 v[34:49], v[90:93], v[240:243], v[34:49]
	ds_read_b128 v[168:171], v179 offset:34144
	v_pk_fma_f16 v55, v55, s55, v233 op_sel_hi:[1,0,0]
	v_pk_fma_f16 v54, v54, s55, v233 op_sel_hi:[1,0,0]
	v_pk_max_f16 v53, v53, v55
	v_pk_max_f16 v52, v52, v54
	s_waitcnt lgkmcnt(5)
	v_mfma_f32_32x32x16_f16 v[34:49], v[118:121], v[244:247], v[34:49]
	ds_read_b128 v[240:243], v179 offset:34176
	v_cvt_pk_f16_f32 v172, v26, v27
	v_cvt_pk_f16_f32 v173, v28, v29
	v_mfma_f32_16x16x32_f16 v[62:65], v[70:73], v[50:53], 0
	s_waitcnt lgkmcnt(5)
	v_mfma_f32_32x32x16_f16 v[34:49], v[78:81], v[18:21], v[34:49]
	ds_read_b128 v[26:29], v179 offset:34208
	v_exp_f16_e64 v244, v172 clamp
	v_exp_f16_e64 v245, v173 clamp
	v_exp_f16_sdwa v244, v172 clamp dst_sel:WORD_1 dst_unused:UNUSED_PRESERVE src0_sel:WORD_1
	v_exp_f16_sdwa v245, v173 clamp dst_sel:WORD_1 dst_unused:UNUSED_PRESERVE src0_sel:WORD_1
	s_nop 0
	s_waitcnt lgkmcnt(5)
	v_mfma_f32_32x32x16_f16 v[34:49], v[102:105], v[248:251], v[34:49]
	ds_read_b128 v[18:21], v179 offset:34240
	v_pk_fma_f16 v245, v245, s55, v233 op_sel_hi:[1,0,0]
	s_nop 0
	v_pk_max_f16 v245, v173, v245
	v_pk_fma_f16 v173, v244, s55, v233 op_sel_hi:[1,0,0]
	s_nop 0
	v_pk_max_f16 v244, v172, v173
	s_waitcnt lgkmcnt(5)
	v_mfma_f32_32x32x16_f16 v[34:49], v[74:77], v[252:255], v[34:49]
	ds_read_b128 v[248:251], v179 offset:34272
	v_cvt_pk_f16_f32 v30, v30, v31
	v_cvt_pk_f16_f32 v31, v32, v33
	s_waitcnt lgkmcnt(5)
	v_mfma_f32_32x32x16_f16 v[34:49], v[106:109], v[22:25], v[34:49]
	v_exp_f16_e64 v32, v30 clamp
	v_exp_f16_e64 v33, v31 clamp
	v_exp_f16_sdwa v32, v30 clamp dst_sel:WORD_1 dst_unused:UNUSED_PRESERVE src0_sel:WORD_1
	v_exp_f16_sdwa v33, v31 clamp dst_sel:WORD_1 dst_unused:UNUSED_PRESERVE src0_sel:WORD_1
	s_nop 0
	s_waitcnt lgkmcnt(4)
	v_mfma_f32_32x32x16_f16 v[34:49], v[82:85], v[168:171], v[34:49]
	v_pk_fma_f16 v22, v33, s55, v233 op_sel_hi:[1,0,0]
	s_nop 0
	v_pk_max_f16 v247, v31, v22
	v_pk_fma_f16 v22, v32, s55, v233 op_sel_hi:[1,0,0]
	s_nop 0
	v_pk_max_f16 v246, v30, v22
	s_waitcnt lgkmcnt(3)
	v_mfma_f32_32x32x16_f16 v[34:49], v[110:113], v[240:243], v[34:49]
	s_waitcnt vmcnt(2)
	v_pk_add_f16 v24, v146, v158
	v_pk_add_f16 v25, v147, v159
	s_nop 0
	v_pk_mul_f16 v22, v160, v148 clamp
	v_pk_mul_f16 v23, v161, v149 clamp
	v_pk_max_f16 v22, v24, v22
	v_pk_max_f16 v23, v25, v23
	ds_write_b64 v189, v[22:23]
	v_mfma_f32_16x16x32_f16 v[62:65], v[66:69], v[244:247], v[62:65]
	s_waitcnt lgkmcnt(3)
	v_mfma_f32_32x32x16_f16 v[34:49], v[94:97], v[26:29], v[34:49]
	v_pk_add_f16 v24, v138, v158
	v_pk_add_f16 v25, v139, v159
	s_nop 0
	v_pk_mul_f16 v22, v160, v140 clamp
	v_pk_mul_f16 v23, v161, v141 clamp
	v_pk_max_f16 v22, v24, v22
	v_pk_max_f16 v23, v25, v23
	ds_write_b64 v189, v[22:23] offset:528
	s_waitcnt lgkmcnt(3)
	v_mfma_f32_32x32x16_f16 v[34:49], v[134:137], v[18:21], v[34:49]
	v_pk_add_f16 v24, v150, v158
	v_pk_add_f16 v25, v151, v159
	s_nop 0
	v_pk_mul_f16 v22, v160, v152 clamp
	v_pk_mul_f16 v23, v161, v153 clamp
	v_pk_max_f16 v22, v24, v22
	v_pk_max_f16 v23, v25, v23
	ds_write_b64 v189, v[22:23] offset:1056
	s_waitcnt lgkmcnt(3)
	v_mfma_f32_32x32x16_f16 v[34:49], v[130:133], v[248:251], v[34:49]
	v_pk_add_f16 v20, v142, v158
	v_pk_add_f16 v21, v143, v159
	s_nop 0
	v_pk_mul_f16 v18, v160, v144 clamp
	v_pk_mul_f16 v19, v161, v145 clamp
	v_pk_max_f16 v18, v20, v18
	v_pk_max_f16 v19, v21, v19
	ds_write_b64 v189, v[18:19] offset:1584
	ds_write2_b32 v201, v62, v63 offset1:1
	s_and_saveexec_b64 s[30:31], s[0:1]
	ds_write2_b32 v201, v64, v65 offset0:2 offset1:3
	s_or_b64 exec, exec, s[30:31]
	v_lshl_add_u64 v[166:167], s[20:21], 4, v[166:167]
	global_load_dwordx4 v[158:161], v[166:167], off
	ds_read_b128 v[50:53], v179 offset:50688
	ds_read_b128 v[54:57], v179 offset:50720
	ds_read_b128 v[58:61], v179 offset:50752
	ds_read_b128 v[62:65], v179 offset:50784
	ds_read_b128 v[168:171], v179 offset:50816
	ds_read_b128 v[240:243], v179 offset:50848
	s_waitcnt lgkmcnt(5)
	v_mfma_f32_32x32x16_f16 v[18:33], v[122:125], v[50:53], v[2:17]
	ds_read_b128 v[244:247], v179 offset:50880
	v_cvt_pk_f16_f32 v172, v34, v35
	v_cvt_pk_f16_f32 v173, v36, v37
	s_waitcnt lgkmcnt(5)
	v_mfma_f32_32x32x16_f16 v[18:33], v[98:101], v[54:57], v[18:33]
	ds_read_b128 v[34:37], v179 offset:50912
	v_exp_f16_e64 v50, v172 clamp
	v_exp_f16_e64 v51, v173 clamp
	v_exp_f16_sdwa v50, v172 clamp dst_sel:WORD_1 dst_unused:UNUSED_PRESERVE src0_sel:WORD_1
	v_exp_f16_sdwa v51, v173 clamp dst_sel:WORD_1 dst_unused:UNUSED_PRESERVE src0_sel:WORD_1
	s_nop 0
	s_waitcnt lgkmcnt(5)
	v_mfma_f32_32x32x16_f16 v[18:33], v[114:117], v[58:61], v[18:33]
	ds_read_b128 v[248:251], v179 offset:50944
	v_pk_fma_f16 v51, v51, s55, v233 op_sel_hi:[1,0,0]
	v_pk_fma_f16 v50, v50, s55, v233 op_sel_hi:[1,0,0]
	v_pk_max_f16 v51, v173, v51
	v_pk_max_f16 v50, v172, v50
	s_waitcnt lgkmcnt(5)
	v_mfma_f32_32x32x16_f16 v[18:33], v[86:89], v[62:65], v[18:33]
	ds_read_b128 v[252:255], v179 offset:50976
	v_cvt_pk_f16_f32 v52, v38, v39
	v_cvt_pk_f16_f32 v53, v40, v41
	s_waitcnt lgkmcnt(5)
	v_mfma_f32_32x32x16_f16 v[18:33], v[126:129], v[168:171], v[18:33]
	ds_read_b128 v[38:41], v179 offset:51008
	v_exp_f16_e64 v54, v52 clamp
	v_exp_f16_e64 v55, v53 clamp
	v_exp_f16_sdwa v54, v52 clamp dst_sel:WORD_1 dst_unused:UNUSED_PRESERVE src0_sel:WORD_1
	v_exp_f16_sdwa v55, v53 clamp dst_sel:WORD_1 dst_unused:UNUSED_PRESERVE src0_sel:WORD_1
	s_nop 0
	s_waitcnt lgkmcnt(5)
	v_mfma_f32_32x32x16_f16 v[18:33], v[90:93], v[240:243], v[18:33]
	ds_read_b128 v[168:171], v179 offset:51040
	v_pk_fma_f16 v55, v55, s55, v233 op_sel_hi:[1,0,0]
	v_pk_fma_f16 v54, v54, s55, v233 op_sel_hi:[1,0,0]
	v_pk_max_f16 v53, v53, v55
	v_pk_max_f16 v52, v52, v54
	s_waitcnt lgkmcnt(5)
	v_mfma_f32_32x32x16_f16 v[18:33], v[118:121], v[244:247], v[18:33]
	ds_read_b128 v[240:243], v179 offset:51072
	v_cvt_pk_f16_f32 v172, v42, v43
	v_cvt_pk_f16_f32 v173, v44, v45
	v_mfma_f32_16x16x32_f16 v[62:65], v[70:73], v[50:53], 0
	s_waitcnt lgkmcnt(5)
	v_mfma_f32_32x32x16_f16 v[18:33], v[78:81], v[34:37], v[18:33]
	ds_read_b128 v[42:45], v179 offset:51104
	v_exp_f16_e64 v244, v172 clamp
	v_exp_f16_e64 v245, v173 clamp
	v_exp_f16_sdwa v244, v172 clamp dst_sel:WORD_1 dst_unused:UNUSED_PRESERVE src0_sel:WORD_1
	v_exp_f16_sdwa v245, v173 clamp dst_sel:WORD_1 dst_unused:UNUSED_PRESERVE src0_sel:WORD_1
	s_nop 0
	s_waitcnt lgkmcnt(5)
	v_mfma_f32_32x32x16_f16 v[18:33], v[102:105], v[248:251], v[18:33]
	ds_read_b128 v[34:37], v179 offset:51136
	v_pk_fma_f16 v245, v245, s55, v233 op_sel_hi:[1,0,0]
	s_nop 0
	v_pk_max_f16 v245, v173, v245
	v_pk_fma_f16 v173, v244, s55, v233 op_sel_hi:[1,0,0]
	s_nop 0
	v_pk_max_f16 v244, v172, v173
	s_waitcnt lgkmcnt(5)
	v_mfma_f32_32x32x16_f16 v[18:33], v[74:77], v[252:255], v[18:33]
	ds_read_b128 v[248:251], v179 offset:51168
	v_cvt_pk_f16_f32 v46, v46, v47
	v_cvt_pk_f16_f32 v47, v48, v49
	s_waitcnt lgkmcnt(5)
	v_mfma_f32_32x32x16_f16 v[18:33], v[106:109], v[38:41], v[18:33]
	v_exp_f16_e64 v48, v46 clamp
	v_exp_f16_e64 v49, v47 clamp
	v_exp_f16_sdwa v48, v46 clamp dst_sel:WORD_1 dst_unused:UNUSED_PRESERVE src0_sel:WORD_1
	v_exp_f16_sdwa v49, v47 clamp dst_sel:WORD_1 dst_unused:UNUSED_PRESERVE src0_sel:WORD_1
	s_nop 0
	s_waitcnt lgkmcnt(4)
	v_mfma_f32_32x32x16_f16 v[18:33], v[82:85], v[168:171], v[18:33]
	v_pk_fma_f16 v38, v49, s55, v233 op_sel_hi:[1,0,0]
	s_nop 0
	v_pk_max_f16 v247, v47, v38
	v_pk_fma_f16 v38, v48, s55, v233 op_sel_hi:[1,0,0]
	s_nop 0
	v_pk_max_f16 v246, v46, v38
	s_waitcnt lgkmcnt(3)
	v_mfma_f32_32x32x16_f16 v[18:33], v[110:113], v[240:243], v[18:33]
	s_waitcnt vmcnt(2)
	v_pk_add_f16 v40, v146, v162
	v_pk_add_f16 v41, v147, v163
	s_nop 0
	v_pk_mul_f16 v38, v164, v148 clamp
	v_pk_mul_f16 v39, v165, v149 clamp
	v_pk_max_f16 v38, v40, v38
	v_pk_max_f16 v39, v41, v39
	ds_write_b64 v189, v[38:39] offset:16896
	v_mfma_f32_16x16x32_f16 v[62:65], v[66:69], v[244:247], v[62:65]
	s_waitcnt lgkmcnt(3)
	v_mfma_f32_32x32x16_f16 v[18:33], v[94:97], v[42:45], v[18:33]
	v_pk_add_f16 v40, v138, v162
	v_pk_add_f16 v41, v139, v163
	s_nop 0
	v_pk_mul_f16 v38, v164, v140 clamp
	v_pk_mul_f16 v39, v165, v141 clamp
	v_pk_max_f16 v38, v40, v38
	v_pk_max_f16 v39, v41, v39
	ds_write_b64 v189, v[38:39] offset:17424
	s_waitcnt lgkmcnt(3)
	v_mfma_f32_32x32x16_f16 v[18:33], v[134:137], v[34:37], v[18:33]
	v_pk_add_f16 v40, v150, v162
	v_pk_add_f16 v41, v151, v163
	s_nop 0
	v_pk_mul_f16 v38, v164, v152 clamp
	v_pk_mul_f16 v39, v165, v153 clamp
	v_pk_max_f16 v38, v40, v38
	v_pk_max_f16 v39, v41, v39
	ds_write_b64 v189, v[38:39] offset:17952
	s_waitcnt lgkmcnt(3)
	v_mfma_f32_32x32x16_f16 v[18:33], v[130:133], v[248:251], v[18:33]
	v_pk_add_f16 v36, v142, v162
	v_pk_add_f16 v37, v143, v163
	s_nop 0
	v_pk_mul_f16 v34, v164, v144 clamp
	v_pk_mul_f16 v35, v165, v145 clamp
	v_pk_max_f16 v34, v36, v34
	v_pk_max_f16 v35, v37, v35
	ds_write_b64 v189, v[34:35] offset:18480
	ds_write2_b32 v211, v62, v63 offset1:1
	s_and_saveexec_b64 s[30:31], s[0:1]
	ds_write2_b32 v211, v64, v65 offset0:2 offset1:3
	s_or_b64 exec, exec, s[30:31]
	s_add_i32 s35, s34, 1
	s_add_i32 s34, s56, 8
	s_cmp_eq_u32 s56, 8
	s_cselect_b64 vcc, -1, 0
	s_and_b64 s[30:31], vcc, exec
	v_lshl_add_u64 v[34:35], s[20:21], 4, v[166:167]
	s_cselect_b32 s20, s44, s20
	s_add_i32 s35, s35, 1
	s_and_b64 s[26:27], exec, s[26:27]
	s_cselect_b32 s30, s51, s35
	s_sub_i32 s26, 0x7e, s30
	s_mul_i32 s26, s26, 6
	s_ashr_i32 s27, s26, 31
	s_add_u32 s26, s28, s26
	s_addc_u32 s27, s29, s27
	s_add_i32 s31, s30, 1
	s_add_i32 s48, s48, 2
	s_add_i32 s54, s54, 16
	v_cndmask_b32_e32 v169, v35, v175, vcc
	v_cndmask_b32_e32 v168, v34, v174, vcc
	s_cmp_eq_u32 s34, 32
	s_waitcnt lgkmcnt(0)
	s_barrier
	s_cbranch_scc1 .LBB1_155
	ds_read_b128 v[50:53], v179
	s_mov_b32 s56, s34
	s_and_b64 vcc, exec, s[8:9]
	s_cbranch_vccz .LBB1_42
	s_branch .LBB1_50
.LBB1_155:
	ds_read_b128 v[50:53], v179
	s_and_b64 vcc, exec, s[24:25]
	s_cbranch_vccz .LBB1_164
	s_cmp_lg_u32 s41, 0
	s_cbranch_scc0 .LBB1_160
	s_and_saveexec_b64 s[12:13], s[6:7]
	s_cbranch_execz .LBB1_159
	ds_read2_b32 v[34:35], v200 offset1:224
	v_add_u32_e32 v36, 0x700, v200
	v_add_u32_e32 v38, 0xe00, v200
	ds_read2_b32 v[36:37], v36 offset1:224
	ds_read2_b32 v[38:39], v38 offset1:224
	s_waitcnt lgkmcnt(2)
	v_add_f32_e32 v34, 0, v34
	v_add_f32_e32 v40, v34, v35
	v_add_u32_e32 v34, 0x1500, v200
	ds_read2_b32 v[34:35], v34 offset1:224
	s_waitcnt lgkmcnt(2)
	v_add_f32_e32 v36, v40, v36
	v_add_f32_e32 v36, v36, v37
	s_waitcnt lgkmcnt(1)
	v_add_f32_e32 v36, v36, v38
	v_add_f32_e32 v36, v36, v39
	s_waitcnt lgkmcnt(0)
	v_add_f32_e32 v34, v36, v34
	v_add_f32_e32 v34, v34, v35
	v_mov_b32_e32 v35, 0x19080
	v_lshl_add_u32 v35, v177, 2, v35
	ds_write_b32 v35, v34

.LBB1_173:
	ds_read_b128 v[54:57], v179 offset:32
	ds_read_b128 v[58:61], v179 offset:64
	ds_read_b128 v[62:65], v179 offset:96
	ds_read_b128 v[162:165], v179 offset:128
	ds_read_b128 v[166:169], v179 offset:160
	s_waitcnt lgkmcnt(5)
	v_mfma_f32_32x32x16_f16 v[34:49], v[122:125], v[50:53], v[2:17]
	ds_read_b128 v[170:173], v179 offset:192
	v_cvt_pk_f16_f32 v174, v18, v19
	v_cvt_pk_f16_f32 v175, v20, v21
	s_waitcnt lgkmcnt(5)
	v_mfma_f32_32x32x16_f16 v[34:49], v[98:101], v[54:57], v[34:49]
	ds_read_b128 v[18:21], v179 offset:224
	v_exp_f16_e64 v50, v174 clamp
	v_exp_f16_e64 v51, v175 clamp
	v_exp_f16_sdwa v50, v174 clamp dst_sel:WORD_1 dst_unused:UNUSED_PRESERVE src0_sel:WORD_1
	v_exp_f16_sdwa v51, v175 clamp dst_sel:WORD_1 dst_unused:UNUSED_PRESERVE src0_sel:WORD_1
	s_nop 0
	s_waitcnt lgkmcnt(5)
	v_mfma_f32_32x32x16_f16 v[34:49], v[114:117], v[58:61], v[34:49]
	ds_read_b128 v[230:233], v179 offset:256
	s_movk_i32 s20, 0x3dc5
	v_mov_b32_e32 v199, 0xbdc5
	v_pk_fma_f16 v51, v51, s20, v199 op_sel_hi:[1,0,0]
	v_pk_fma_f16 v50, v50, s20, v199 op_sel_hi:[1,0,0]
	v_pk_max_f16 v51, v175, v51
	v_pk_max_f16 v50, v174, v50
	s_waitcnt lgkmcnt(5)
	v_mfma_f32_32x32x16_f16 v[34:49], v[86:89], v[62:65], v[34:49]
	ds_read_b128 v[234:237], v179 offset:288
	v_cvt_pk_f16_f32 v52, v22, v23
	v_cvt_pk_f16_f32 v53, v24, v25
	s_waitcnt lgkmcnt(5)
	v_mfma_f32_32x32x16_f16 v[34:49], v[126:129], v[162:165], v[34:49]
	ds_read_b128 v[22:25], v179 offset:320
	v_exp_f16_e64 v54, v52 clamp
	v_exp_f16_e64 v55, v53 clamp
	v_exp_f16_sdwa v54, v52 clamp dst_sel:WORD_1 dst_unused:UNUSED_PRESERVE src0_sel:WORD_1
	v_exp_f16_sdwa v55, v53 clamp dst_sel:WORD_1 dst_unused:UNUSED_PRESERVE src0_sel:WORD_1
	s_nop 0
	s_waitcnt lgkmcnt(5)
	v_mfma_f32_32x32x16_f16 v[34:49], v[90:93], v[166:169], v[34:49]
	ds_read_b128 v[162:165], v179 offset:352
	v_pk_fma_f16 v55, v55, s20, v199 op_sel_hi:[1,0,0]
	v_pk_fma_f16 v54, v54, s20, v199 op_sel_hi:[1,0,0]
	v_pk_max_f16 v53, v53, v55
	v_pk_max_f16 v52, v52, v54
	s_waitcnt lgkmcnt(5)
	v_mfma_f32_32x32x16_f16 v[34:49], v[118:121], v[170:173], v[34:49]
	ds_read_b128 v[166:169], v179 offset:384
	v_cvt_pk_f16_f32 v170, v26, v27
	v_cvt_pk_f16_f32 v171, v28, v29
	v_mfma_f32_16x16x32_f16 v[62:65], v[70:73], v[50:53], 0
	s_waitcnt lgkmcnt(5)
	v_mfma_f32_32x32x16_f16 v[34:49], v[78:81], v[18:21], v[34:49]
	ds_read_b128 v[26:29], v179 offset:416
	v_exp_f16_e64 v172, v170 clamp
	v_exp_f16_e64 v173, v171 clamp
	v_exp_f16_sdwa v172, v170 clamp dst_sel:WORD_1 dst_unused:UNUSED_PRESERVE src0_sel:WORD_1
	v_exp_f16_sdwa v173, v171 clamp dst_sel:WORD_1 dst_unused:UNUSED_PRESERVE src0_sel:WORD_1
	s_nop 0
	s_waitcnt lgkmcnt(5)
	v_mfma_f32_32x32x16_f16 v[34:49], v[102:105], v[230:233], v[34:49]
	ds_read_b128 v[18:21], v179 offset:448
	v_pk_fma_f16 v173, v173, s20, v199 op_sel_hi:[1,0,0]
	v_pk_fma_f16 v172, v172, s20, v199 op_sel_hi:[1,0,0]
	v_pk_max_f16 v171, v171, v173
	v_pk_max_f16 v170, v170, v172
	s_waitcnt lgkmcnt(5)
	v_mfma_f32_32x32x16_f16 v[34:49], v[74:77], v[234:237], v[34:49]
	ds_read_b128 v[230:233], v179 offset:480
	v_cvt_pk_f16_f32 v30, v30, v31
	v_cvt_pk_f16_f32 v31, v32, v33
	s_waitcnt lgkmcnt(5)
	v_mfma_f32_32x32x16_f16 v[34:49], v[106:109], v[22:25], v[34:49]
	v_exp_f16_e64 v32, v30 clamp
	v_exp_f16_e64 v33, v31 clamp
	v_exp_f16_sdwa v32, v30 clamp dst_sel:WORD_1 dst_unused:UNUSED_PRESERVE src0_sel:WORD_1
	v_exp_f16_sdwa v33, v31 clamp dst_sel:WORD_1 dst_unused:UNUSED_PRESERVE src0_sel:WORD_1
	s_nop 0
	s_waitcnt lgkmcnt(4)
	v_mfma_f32_32x32x16_f16 v[34:49], v[82:85], v[162:165], v[34:49]
	v_pk_fma_f16 v22, v33, s20, v199 op_sel_hi:[1,0,0]
	s_nop 0
	v_pk_max_f16 v173, v31, v22
	v_pk_fma_f16 v22, v32, s20, v199 op_sel_hi:[1,0,0]
	s_nop 0
	v_pk_max_f16 v172, v30, v22
	s_waitcnt lgkmcnt(3)
	v_mfma_f32_32x32x16_f16 v[34:49], v[110:113], v[166:169], v[34:49]
	s_waitcnt vmcnt(1)
	v_pk_add_f16 v24, v146, v154
	v_pk_add_f16 v25, v147, v155
	s_nop 0
	v_pk_mul_f16 v22, v156, v148 clamp
	v_pk_mul_f16 v23, v157, v149 clamp
	v_pk_max_f16 v22, v24, v22
	v_pk_max_f16 v23, v25, v23
	ds_write_b64 v189, v[22:23] offset:33792
	v_mfma_f32_16x16x32_f16 v[62:65], v[66:69], v[170:173], v[62:65]
	s_waitcnt lgkmcnt(3)
	v_mfma_f32_32x32x16_f16 v[34:49], v[94:97], v[26:29], v[34:49]
	v_pk_add_f16 v24, v138, v154
	v_pk_add_f16 v25, v139, v155
	s_nop 0
	v_pk_mul_f16 v22, v156, v140 clamp
	v_pk_mul_f16 v23, v157, v141 clamp
	v_pk_max_f16 v22, v24, v22
	v_pk_max_f16 v23, v25, v23
	ds_write_b64 v189, v[22:23] offset:34320
	s_waitcnt lgkmcnt(3)
	v_mfma_f32_32x32x16_f16 v[34:49], v[134:137], v[18:21], v[34:49]
	v_pk_add_f16 v24, v150, v154
	v_pk_add_f16 v25, v151, v155
	s_nop 0
	v_pk_mul_f16 v22, v156, v152 clamp
	v_pk_mul_f16 v23, v157, v153 clamp
	v_pk_max_f16 v22, v24, v22
	v_pk_max_f16 v23, v25, v23
	ds_write_b64 v189, v[22:23] offset:34848
	s_waitcnt lgkmcnt(3)
	v_mfma_f32_32x32x16_f16 v[34:49], v[130:133], v[230:233], v[34:49]
	v_pk_add_f16 v20, v142, v154
	v_pk_add_f16 v21, v143, v155
	s_nop 0
	v_pk_mul_f16 v18, v156, v144 clamp
	v_pk_mul_f16 v19, v157, v145 clamp
	v_pk_max_f16 v18, v20, v18
	v_pk_max_f16 v19, v21, v19
	ds_write_b64 v189, v[18:19] offset:35376
	ds_write2_b32 v229, v62, v63 offset1:1
	s_and_saveexec_b64 s[20:21], s[0:1]
	ds_write2_b32 v229, v64, v65 offset0:2 offset1:3
	s_or_b64 exec, exec, s[20:21]
	ds_read_b128 v[50:53], v179 offset:16896
	ds_read_b128 v[54:57], v179 offset:16928
	ds_read_b128 v[58:61], v179 offset:16960
	ds_read_b128 v[62:65], v179 offset:16992
	ds_read_b128 v[154:157], v179 offset:17024
	ds_read_b128 v[162:165], v179 offset:17056
	s_waitcnt lgkmcnt(5)
	v_mfma_f32_32x32x16_f16 v[18:33], v[122:125], v[50:53], v[2:17]
	ds_read_b128 v[166:169], v179 offset:17088
	v_cvt_pk_f16_f32 v174, v34, v35
	v_cvt_pk_f16_f32 v175, v36, v37
	s_waitcnt lgkmcnt(5)
	v_mfma_f32_32x32x16_f16 v[18:33], v[98:101], v[54:57], v[18:33]
	ds_read_b128 v[34:37], v179 offset:17120
	v_exp_f16_e64 v50, v174 clamp
	v_exp_f16_e64 v51, v175 clamp
	v_exp_f16_sdwa v50, v174 clamp dst_sel:WORD_1 dst_unused:UNUSED_PRESERVE src0_sel:WORD_1
	v_exp_f16_sdwa v51, v175 clamp dst_sel:WORD_1 dst_unused:UNUSED_PRESERVE src0_sel:WORD_1
	s_nop 0
	s_waitcnt lgkmcnt(5)
	v_mfma_f32_32x32x16_f16 v[18:33], v[114:117], v[58:61], v[18:33]
	ds_read_b128 v[170:173], v179 offset:17152
	s_movk_i32 s20, 0x3dc5
	v_mov_b32_e32 v199, 0xbdc5
	v_pk_fma_f16 v51, v51, s20, v199 op_sel_hi:[1,0,0]
	v_pk_fma_f16 v50, v50, s20, v199 op_sel_hi:[1,0,0]
	v_pk_max_f16 v51, v175, v51
	v_pk_max_f16 v50, v174, v50
	s_waitcnt lgkmcnt(5)
	v_mfma_f32_32x32x16_f16 v[18:33], v[86:89], v[62:65], v[18:33]
	ds_read_b128 v[228:231], v179 offset:17184
	v_cvt_pk_f16_f32 v52, v38, v39
	v_cvt_pk_f16_f32 v53, v40, v41
	s_waitcnt lgkmcnt(5)
	v_mfma_f32_32x32x16_f16 v[18:33], v[126:129], v[154:157], v[18:33]
	ds_read_b128 v[38:41], v179 offset:17216
	v_exp_f16_e64 v54, v52 clamp
	v_exp_f16_e64 v55, v53 clamp
	v_exp_f16_sdwa v54, v52 clamp dst_sel:WORD_1 dst_unused:UNUSED_PRESERVE src0_sel:WORD_1
	v_exp_f16_sdwa v55, v53 clamp dst_sel:WORD_1 dst_unused:UNUSED_PRESERVE src0_sel:WORD_1
	s_nop 0
	s_waitcnt lgkmcnt(5)
	v_mfma_f32_32x32x16_f16 v[18:33], v[90:93], v[162:165], v[18:33]
	ds_read_b128 v[154:157], v179 offset:17248
	v_pk_fma_f16 v55, v55, s20, v199 op_sel_hi:[1,0,0]
	v_pk_fma_f16 v54, v54, s20, v199 op_sel_hi:[1,0,0]
	v_pk_max_f16 v53, v53, v55
	v_pk_max_f16 v52, v52, v54
	s_waitcnt lgkmcnt(5)
	v_mfma_f32_32x32x16_f16 v[18:33], v[118:121], v[166:169], v[18:33]
	ds_read_b128 v[162:165], v179 offset:17280
	v_cvt_pk_f16_f32 v166, v42, v43
	v_cvt_pk_f16_f32 v167, v44, v45
	v_mfma_f32_16x16x32_f16 v[62:65], v[70:73], v[50:53], 0
	s_waitcnt lgkmcnt(5)
	v_mfma_f32_32x32x16_f16 v[18:33], v[78:81], v[34:37], v[18:33]
	ds_read_b128 v[42:45], v179 offset:17312
	v_exp_f16_e64 v168, v166 clamp
	v_exp_f16_e64 v169, v167 clamp
	v_exp_f16_sdwa v168, v166 clamp dst_sel:WORD_1 dst_unused:UNUSED_PRESERVE src0_sel:WORD_1
	v_exp_f16_sdwa v169, v167 clamp dst_sel:WORD_1 dst_unused:UNUSED_PRESERVE src0_sel:WORD_1
	s_nop 0
	s_waitcnt lgkmcnt(5)
	v_mfma_f32_32x32x16_f16 v[18:33], v[102:105], v[170:173], v[18:33]
	ds_read_b128 v[34:37], v179 offset:17344
	v_pk_fma_f16 v169, v169, s20, v199 op_sel_hi:[1,0,0]
	v_pk_fma_f16 v168, v168, s20, v199 op_sel_hi:[1,0,0]
	v_pk_max_f16 v167, v167, v169
	v_pk_max_f16 v166, v166, v168
	s_waitcnt lgkmcnt(5)
	v_mfma_f32_32x32x16_f16 v[18:33], v[74:77], v[228:231], v[18:33]
	ds_read_b128 v[170:173], v179 offset:17376
	v_cvt_pk_f16_f32 v46, v46, v47
	v_cvt_pk_f16_f32 v47, v48, v49
	s_waitcnt lgkmcnt(5)
	v_mfma_f32_32x32x16_f16 v[18:33], v[106:109], v[38:41], v[18:33]
	v_exp_f16_e64 v48, v46 clamp
	v_exp_f16_e64 v49, v47 clamp
	v_exp_f16_sdwa v48, v46 clamp dst_sel:WORD_1 dst_unused:UNUSED_PRESERVE src0_sel:WORD_1
	v_exp_f16_sdwa v49, v47 clamp dst_sel:WORD_1 dst_unused:UNUSED_PRESERVE src0_sel:WORD_1
	s_nop 0
	s_waitcnt lgkmcnt(4)
	v_mfma_f32_32x32x16_f16 v[18:33], v[82:85], v[154:157], v[18:33]
	v_pk_fma_f16 v38, v49, s20, v199 op_sel_hi:[1,0,0]
	s_nop 0
	v_pk_max_f16 v169, v47, v38
	v_pk_fma_f16 v38, v48, s20, v199 op_sel_hi:[1,0,0]
	s_nop 0
	v_pk_max_f16 v168, v46, v38
	s_waitcnt lgkmcnt(3)
	v_mfma_f32_32x32x16_f16 v[18:33], v[110:113], v[162:165], v[18:33]
	s_waitcnt vmcnt(0)
	v_pk_add_f16 v40, v146, v158
	v_pk_add_f16 v41, v147, v159
	s_nop 0
	v_pk_mul_f16 v38, v160, v148 clamp
	v_pk_mul_f16 v39, v161, v149 clamp
	v_pk_max_f16 v38, v40, v38
	v_pk_max_f16 v39, v41, v39
	ds_write_b64 v189, v[38:39] offset:50688
	v_mfma_f32_16x16x32_f16 v[62:65], v[66:69], v[166:169], v[62:65]
	s_waitcnt lgkmcnt(3)
	v_mfma_f32_32x32x16_f16 v[18:33], v[94:97], v[42:45], v[18:33]
	v_pk_add_f16 v40, v138, v158
	v_pk_add_f16 v41, v139, v159
	s_nop 0
	v_pk_mul_f16 v38, v160, v140 clamp
	v_pk_mul_f16 v39, v161, v141 clamp
	v_pk_max_f16 v38, v40, v38
	v_pk_max_f16 v39, v41, v39
	ds_write_b64 v189, v[38:39] offset:51216
	s_waitcnt lgkmcnt(3)
	v_mfma_f32_32x32x16_f16 v[18:33], v[134:137], v[34:37], v[18:33]
	v_pk_add_f16 v40, v150, v158
	v_pk_add_f16 v41, v151, v159
	s_nop 0
	v_pk_mul_f16 v38, v160, v152 clamp
	v_pk_mul_f16 v39, v161, v153 clamp
	v_pk_max_f16 v38, v40, v38
	v_pk_max_f16 v39, v41, v39
	ds_write_b64 v189, v[38:39] offset:51744
	s_waitcnt lgkmcnt(3)
	v_mfma_f32_32x32x16_f16 v[18:33], v[130:133], v[170:173], v[18:33]
	v_pk_add_f16 v36, v142, v158
	v_pk_add_f16 v37, v143, v159
	s_nop 0
	v_pk_mul_f16 v34, v160, v144 clamp
	v_pk_mul_f16 v35, v161, v145 clamp
	v_pk_max_f16 v34, v36, v34
	v_pk_max_f16 v35, v37, v35
	ds_write_b64 v189, v[34:35] offset:52272
	ds_write2_b32 v206, v62, v63 offset1:1
	s_and_saveexec_b64 s[20:21], s[0:1]
	ds_write2_b32 v206, v64, v65 offset0:2 offset1:3
	s_or_b64 exec, exec, s[20:21]
	s_sub_i32 s20, 0x7c, s30
	s_mul_i32 s20, s20, 6
	s_ashr_i32 s21, s20, 31
	s_add_u32 s12, s12, s20
	s_addc_u32 s13, s13, s21
	s_and_b64 vcc, exec, s[8:9]
	s_waitcnt lgkmcnt(0)
	s_barrier
	s_cbranch_vccnz .LBB1_190
	s_cmp_lg_u32 s41, 0
	s_cbranch_scc0 .LBB1_186
	s_and_saveexec_b64 s[20:21], s[6:7]
	s_cbranch_execz .LBB1_185
	ds_read2_b32 v[34:35], v180 offset1:224
	v_add_u32_e32 v36, 0x700, v180
	v_add_u32_e32 v38, 0xe00, v180
	ds_read2_b32 v[36:37], v36 offset1:224
	ds_read2_b32 v[38:39], v38 offset1:224
	s_waitcnt lgkmcnt(2)
	v_add_f32_e32 v34, 0, v34
	v_add_f32_e32 v40, v34, v35
	v_add_u32_e32 v34, 0x1500, v180
	ds_read2_b32 v[34:35], v34 offset1:224
	s_waitcnt lgkmcnt(2)
	v_add_f32_e32 v36, v40, v36
	v_add_f32_e32 v36, v36, v37
	s_waitcnt lgkmcnt(1)
	v_add_f32_e32 v36, v36, v38
	v_add_f32_e32 v36, v36, v39
	s_waitcnt lgkmcnt(0)
	v_add_f32_e32 v34, v36, v34
	v_add_f32_e32 v34, v34, v35
	v_mov_b32_e32 v35, 0x19180
	v_lshl_add_u32 v35, v177, 2, v35
	ds_write_b32 v35, v34
